# logsigmoid(gamma) tables built vectorized across lanes (one evaluation) for ret_out and ret_kv, both layers
# speedup vs baseline: 1.0082x; 1.0082x over previous
.LBB0_984:
	s_andn2_b64 vcc, exec, s[10:11]
	s_cbranch_vccnz .LBB0_998
	s_lshl_b32 s10, s8, 4
	s_ashr_i32 s11, s10, 31
	v_readlane_b32 s16, v233, 0
	s_ashr_i32 s9, s12, 8
	s_lshl_b64 s[10:11], s[10:11], 2
	v_readlane_b32 s26, v233, 10
	v_readlane_b32 s27, v233, 11
	s_add_u32 s10, s26, s10
	s_addc_u32 s11, s27, s11
	v_readlane_b32 s17, v233, 1
	s_add_u32 s16, s6, 0x27400000
	s_addc_u32 s17, s7, 0
	s_lshl_b32 s62, s96, 1
	s_add_i32 s13, s9, s62
	s_ashr_i32 s14, s13, 31
	v_readlane_b32 s18, v233, 2
	s_bfe_u32 s3, s12, 0x20006
	s_lshr_b32 s12, s14, 27
	s_add_i32 s18, s13, s12
	s_and_b32 s12, s18, 0xffffffe0
	s_lshr_b32 s14, s14, 24
	s_sub_i32 s12, s13, s12
	s_add_i32 s13, s13, s14
	s_ashr_i32 s14, s13, 8
	s_mul_i32 s2, s9, 0xd800
	s_ashr_i32 s15, s14, 31
	s_ashr_i32 s13, s12, 31
	s_add_i32 s2, s2, 0
	s_lshl_b64 s[14:15], s[14:15], 12
	s_lshl_b64 s[12:13], s[12:13], 7
	s_add_u32 s12, s14, s12
	s_addc_u32 s13, s15, s13
	s_mulk_i32 s13, 0x3400
	s_mul_hi_u32 s14, s12, 0x3400
	s_add_i32 s14, s14, s13
	s_mulk_i32 s12, 0x3400
	s_add_u32 s12, s0, s12
	s_addc_u32 s13, s1, s14
	s_lshl_b32 s14, s18, 2
	s_and_b32 s14, s14, 0x380
	v_bfe_u32 v37, v1, 3, 5
	s_add_u32 s12, s12, s14
	v_mul_u32_u24_e32 v36, 0x1a00, v37
	s_addc_u32 s13, s13, 0
	v_and_b32_e32 v38, 56, v144
	v_mov_b32_e32 v35, 0
	v_lshlrev_b32_e32 v34, 1, v36
	v_lshl_add_u64 v[2:3], s[12:13], 0, v[34:35]
	v_lshlrev_b32_e32 v34, 1, v38
	v_lshl_add_u64 v[26:27], v[2:3], 0, v[34:35]
	s_mov_b32 s12, 0x68000
	v_add_co_u32_e32 v14, vcc, s12, v26
	s_mov_b32 s12, 0xd0000
	s_nop 0
	v_addc_co_u32_e32 v15, vcc, 0, v27, vcc
	v_add_co_u32_e32 v22, vcc, s12, v26
	s_mov_b32 s12, 0x138000
	s_nop 0
	v_addc_co_u32_e32 v23, vcc, 0, v27, vcc
	v_add_co_u32_e32 v30, vcc, s12, v26
	global_load_dwordx4 v[2:5], v[26:27], off offset:1024
	global_load_dwordx4 v[6:9], v[26:27], off offset:2048
	v_addc_co_u32_e32 v31, vcc, 0, v27, vcc
	global_load_dwordx4 v[10:13], v[14:15], off offset:1024
	s_nop 0
	global_load_dwordx4 v[14:17], v[14:15], off offset:2048
	s_nop 0
	global_load_dwordx4 v[18:21], v[22:23], off offset:1024
	s_nop 0
	global_load_dwordx4 v[22:25], v[22:23], off offset:2048
	s_nop 0
	global_load_dwordx4 v[26:29], v[30:31], off offset:1024
	s_nop 0
	global_load_dwordx4 v[30:33], v[30:31], off offset:2048
	v_lshlrev_b32_e32 v43, 6, v146
	v_lshrrev_b32_e32 v40, 3, v1
	s_lshl_b32 s12, s3, 5
	v_lshl_or_b32 v44, s3, 10, v43
	s_movk_i32 s3, 0x7f
	v_bitop3_b32 v43, v40, s3, 31 bitop3:0x6c
	v_cvt_f32_ubyte0_e32 v46, v43
	v_mul_u32_u24_e32 v43, 0x48, v37
	v_lshlrev_b32_e32 v43, 1, v43
	s_movk_i32 s3, 0x5f
	v_add3_u32 v48, s2, v34, v43
	v_bitop3_b32 v43, v40, s3, 31 bitop3:0x6c
	v_lshl_or_b32 v39, v145, 3, v39
	v_cvt_f32_ubyte0_e32 v47, v37
	v_or_b32_e32 v34, 32, v37
	v_cvt_f32_ubyte0_e32 v49, v43
	v_or_b32_e32 v43, 64, v37
	v_or_b32_e32 v37, 0x60, v37
	v_cvt_f32_ubyte0_e32 v54, v37
	v_mul_u32_u24_e32 v37, 0x48, v39
	v_readlane_b32 s19, v233, 3
	v_readlane_b32 s20, v233, 4
	v_readlane_b32 s21, v233, 5
	v_readlane_b32 s22, v233, 6
	v_readlane_b32 s23, v233, 7
	v_readlane_b32 s24, v233, 8
	v_readlane_b32 s25, v233, 9
	v_readlane_b32 s28, v233, 12
	v_readlane_b32 s29, v233, 13
	s_lshl_b32 s18, s90, 1
	s_add_i32 s12, s2, s12
	v_and_b32_e32 v41, 24, v144
	v_lshlrev_b32_e32 v42, 2, v145
	v_cvt_f32_ubyte0_e32 v50, v34
	v_bitop3_b32 v45, v40, 63, 31 bitop3:0x6c
	v_bitop3_b32 v40, v40, 31, v40 bitop3:0xc
	v_mul_u32_u24_e32 v34, 0x1a00, v34
	v_lshlrev_b32_e32 v37, 1, v37
	v_cvt_f32_ubyte0_e32 v51, v45
	v_cvt_f32_ubyte0_e32 v52, v43
	v_cvt_f32_ubyte0_e32 v53, v40
	v_add3_u32 v55, s12, v41, v37
	v_add3_u32 v56, s2, v41, v37
	s_add_i32 s19, s9, s18
	s_mov_b32 s20, 0xbfb8aa3b
	s_mov_b32 s21, 0x42ce8ed0
	s_mov_b32 s22, 0xc2b17218
	s_mov_b32 s23, 0x7f800000
	s_mov_b32 s24, 0x3f2aaaab
	v_mov_b32_e32 v57, 0x3ecc95a3
	s_mov_b32 s25, 0x3f317218
	s_mov_b32 s26, 0x33800000
	s_mov_b32 s27, 0x3fb8aa3b
	s_mov_b32 s28, 0xc2ce8ed0
	s_mov_b32 s29, 0x42b17218
	v_lshlrev_b32_e32 v36, 1, v36
	v_lshlrev_b32_e32 v38, 1, v38
	v_lshlrev_b32_e32 v40, 1, v34
	v_lshlrev_b32_e32 v34, 1, v44
	v_lshlrev_b32_e32 v42, 1, v42
	v_mov_b32_e32 v58, 0x7f800000
	v_mov_b32_e32 v44, 0x3f317218
	s_mov_b32 s36, s62
	v_readlane_b32 s30, v233, 14
	v_readlane_b32 s31, v233, 15
	v_mbcnt_lo_u32_b32 v231, -1, 0
	v_mbcnt_hi_u32_b32 v231, -1, v231
	v_and_b32_e32 v231, 15, v231
	v_lshlrev_b32_e32 v37, 2, v231
	global_load_dword v39, v37, s[10:11]
	s_waitcnt vmcnt(0)
	v_cmp_ngt_f32_e32 vcc, 0, v39
	s_and_saveexec_b64 s[98:99], vcc
	s_cbranch_execz .Llsv_rk0_a
	v_mul_f32_e32 v37, 0xbfb8aa3b, v39
	v_rndne_f32_e32 v41, v37
	v_sub_f32_e32 v43, v37, v41
	v_fma_f32 v37, v39, s20, -v37
	v_fmac_f32_e32 v37, 0xb2a5705f, v39
	v_add_f32_e32 v37, v43, v37
	v_cvt_i32_f32_e32 v41, v41
	v_exp_f32_e32 v37, v37
	v_cmp_nlt_f32_e32 vcc, s21, v39
	v_ldexp_f32 v37, v37, v41
	s_nop 0
	v_cndmask_b32_e32 v37, 0, v37, vcc
	v_cmp_ngt_f32_e32 vcc, s22, v39
	s_nop 1
	v_cndmask_b32_e32 v37, v58, v37, vcc
	v_add_f32_e32 v41, 1.0, v37
	v_add_f32_e32 v43, -1.0, v41
	v_sub_f32_e32 v45, v43, v41
	v_add_f32_e32 v45, 1.0, v45
	v_sub_f32_e32 v43, v37, v43
	v_add_f32_e32 v43, v43, v45
	v_frexp_mant_f32_e32 v45, v41
	v_cvt_f64_f32_e32 v[60:61], v41
	v_frexp_exp_i32_f64_e32 v59, v[60:61]
	v_cmp_gt_f32_e32 vcc, s24, v45
	s_nop 1
	v_subbrev_co_u32_e32 v59, vcc, 0, v59, vcc
	v_sub_u32_e32 v45, 0, v59
	v_ldexp_f32 v41, v41, v45
	v_ldexp_f32 v43, v43, v45
	v_add_f32_e32 v45, -1.0, v41
	v_add_f32_e32 v61, 1.0, v41
	v_add_f32_e32 v60, 1.0, v45
	v_add_f32_e32 v62, -1.0, v61
	v_sub_f32_e32 v60, v41, v60
	v_sub_f32_e32 v41, v41, v62
	v_add_f32_e32 v41, v43, v41
	v_add_f32_e32 v60, v43, v60
	v_add_f32_e32 v43, v61, v41
	v_rcp_f32_e32 v68, v43
	v_sub_f32_e32 v61, v61, v43
	v_add_f32_e32 v41, v41, v61
	v_add_f32_e32 v61, v45, v60
	v_mul_f32_e32 v69, v61, v68
	v_mul_f32_e32 v62, v43, v69
	v_fma_f32 v64, v69, v43, -v62
	v_sub_f32_e32 v45, v45, v61
	v_fmac_f32_e32 v64, v69, v41
	v_add_f32_e32 v45, v60, v45
	v_add_f32_e32 v60, v62, v64
	v_sub_f32_e32 v63, v61, v60
	v_pk_add_f32 v[66:67], v[60:61], v[62:63] neg_lo:[0,1] neg_hi:[0,1]
	v_mov_b32_e32 v65, v60
	v_pk_add_f32 v[60:61], v[66:67], v[64:65] neg_lo:[0,1] neg_hi:[0,1]
	v_cmp_neq_f32_e32 vcc, s23, v37
	v_add_f32_e32 v45, v45, v61
	v_add_f32_e32 v45, v60, v45
	v_add_f32_e32 v61, v63, v45
	v_mul_f32_e32 v70, v68, v61
	v_mul_f32_e32 v62, v43, v70
	v_fma_f32 v64, v70, v43, -v62
	v_fmac_f32_e32 v64, v70, v41
	v_add_f32_e32 v60, v62, v64
	v_sub_f32_e32 v41, v63, v61
	v_sub_f32_e32 v63, v61, v60
	v_pk_add_f32 v[66:67], v[60:61], v[62:63] neg_lo:[0,1] neg_hi:[0,1]
	v_mov_b32_e32 v65, v60
	v_add_f32_e32 v41, v45, v41
	v_pk_add_f32 v[60:61], v[66:67], v[64:65] neg_lo:[0,1] neg_hi:[0,1]
	v_add_f32_e32 v43, v69, v70
	v_add_f32_e32 v41, v41, v61
	v_add_f32_e32 v41, v60, v41
	v_add_f32_e32 v41, v63, v41
	v_sub_f32_e32 v45, v43, v69
	v_mul_f32_e32 v41, v68, v41
	v_sub_f32_e32 v45, v70, v45
	v_add_f32_e32 v41, v45, v41
	v_add_f32_e32 v61, v43, v41
	v_cvt_f32_i32_e32 v60, v59
	v_mul_f32_e32 v62, v61, v61
	v_fmamk_f32 v45, v62, 0x3e9b6dac, v57
	v_fmaak_f32 v45, v62, v45, 0x3f2aaada
	v_sub_f32_e32 v43, v61, v43
	v_ldexp_f32 v63, v61, 1
	v_mul_f32_e32 v61, v61, v62
	v_pk_mul_f32 v[64:65], v[60:61], v[44:45]
	v_sub_f32_e32 v41, v41, v43
	v_fma_f32 v62, v60, s25, -v64
	v_fmac_f32_e32 v62, 0xb102e308, v60
	v_pk_add_f32 v[60:61], v[64:65], v[62:63]
	v_ldexp_f32 v41, v41, 1
	v_sub_f32_e32 v43, v61, v63
	v_sub_f32_e32 v43, v65, v43
	v_add_f32_e32 v67, v41, v43
	v_mov_b32_e32 v66, v64
	v_pk_add_f32 v[64:65], v[60:61], v[64:65] neg_lo:[0,1] neg_hi:[0,1]
	v_pk_add_f32 v[68:69], v[60:61], v[66:67]
	v_mov_b32_e32 v63, v60
	v_mov_b32_e32 v65, v69
	v_pk_add_f32 v[70:71], v[62:63], v[64:65] neg_lo:[0,1] neg_hi:[0,1]
	v_pk_add_f32 v[62:63], v[62:63], v[64:65]
	v_mov_b32_e32 v74, v61
	v_pk_add_f32 v[64:65], v[62:63], v[60:61] op_sel:[1,0] op_sel_hi:[0,1] neg_lo:[0,1] neg_hi:[0,1]
	v_pk_add_f32 v[72:73], v[68:69], v[64:65] op_sel_hi:[1,0] neg_lo:[0,1] neg_hi:[0,1]
	v_mov_b32_e32 v68, v69
	v_mov_b32_e32 v69, v63
	v_mov_b32_e32 v75, v64
	v_pk_add_f32 v[64:65], v[68:69], v[74:75] neg_lo:[0,1] neg_hi:[0,1]
	v_mov_b32_e32 v66, v67
	v_mov_b32_e32 v67, v60
	v_pk_add_f32 v[60:61], v[66:67], v[64:65] neg_lo:[0,1] neg_hi:[0,1]
	v_mov_b32_e32 v72, v70
	v_pk_add_f32 v[64:65], v[72:73], v[60:61]
	v_mov_b32_e32 v71, v63
	v_pk_add_f32 v[66:67], v[64:65], v[64:65] op_sel:[0,1] op_sel_hi:[1,0]
	s_nop 0
	v_pk_add_f32 v[62:63], v[62:63], v[66:67] op_sel:[1,0] op_sel_hi:[0,1]
	v_mov_b32_e32 v65, v62
	v_pk_add_f32 v[68:69], v[64:65], v[70:71] neg_lo:[0,1] neg_hi:[0,1]
	v_mov_b32_e32 v61, v66
	v_sub_f32_e32 v41, v64, v68
	v_pk_add_f32 v[60:61], v[60:61], v[68:69] neg_lo:[0,1] neg_hi:[0,1]
	v_sub_f32_e32 v41, v70, v41
	v_add_f32_e32 v41, v60, v41
	v_add_f32_e32 v41, v41, v61
	v_add_f32_e32 v41, v62, v41
	v_cndmask_b32_e32 v41, v58, v41, vcc
	v_cmp_lt_f32_e64 vcc, |v37|, s26
	s_nop 1
	v_cndmask_b32_e32 v37, v41, v37, vcc
	v_xor_b32_e32 v37, 0x80000000, v37
.Llsv_rk0_a:
	s_xor_b64 exec, exec, s[98:99]
	s_cbranch_execz .Llsv_rk0_b
	v_mul_f32_e32 v37, 0x3fb8aa3b, v39
	v_rndne_f32_e32 v41, v37
	v_sub_f32_e32 v43, v37, v41
	v_fma_f32 v37, v39, s27, -v37
	v_fmac_f32_e32 v37, 0x32a5705f, v39
	v_add_f32_e32 v37, v43, v37
	v_cvt_i32_f32_e32 v41, v41
	v_exp_f32_e32 v37, v37
	v_cmp_ngt_f32_e32 vcc, s28, v39
	v_ldexp_f32 v37, v37, v41
	s_nop 0
	v_cndmask_b32_e32 v37, 0, v37, vcc
	v_cmp_nlt_f32_e32 vcc, s29, v39
	s_nop 1
	v_cndmask_b32_e32 v37, v58, v37, vcc
	v_add_f32_e32 v41, 1.0, v37
	v_add_f32_e32 v43, -1.0, v41
	v_sub_f32_e32 v45, v43, v41
	v_add_f32_e32 v45, 1.0, v45
	v_sub_f32_e32 v43, v37, v43
	v_add_f32_e32 v43, v43, v45
	v_frexp_mant_f32_e32 v45, v41
	v_cvt_f64_f32_e32 v[60:61], v41
	v_frexp_exp_i32_f64_e32 v59, v[60:61]
	v_cmp_gt_f32_e32 vcc, s24, v45
	s_nop 1
	v_subbrev_co_u32_e32 v59, vcc, 0, v59, vcc
	v_sub_u32_e32 v45, 0, v59
	v_ldexp_f32 v41, v41, v45
	v_ldexp_f32 v43, v43, v45
	v_add_f32_e32 v45, -1.0, v41
	v_add_f32_e32 v61, 1.0, v41
	v_add_f32_e32 v60, 1.0, v45
	v_add_f32_e32 v62, -1.0, v61
	v_sub_f32_e32 v60, v41, v60
	v_sub_f32_e32 v41, v41, v62
	v_add_f32_e32 v41, v43, v41
	v_add_f32_e32 v60, v43, v60
	v_add_f32_e32 v43, v61, v41
	v_rcp_f32_e32 v68, v43
	v_sub_f32_e32 v61, v61, v43
	v_add_f32_e32 v41, v41, v61
	v_add_f32_e32 v61, v45, v60
	v_mul_f32_e32 v69, v61, v68
	v_mul_f32_e32 v62, v43, v69
	v_fma_f32 v64, v69, v43, -v62
	v_sub_f32_e32 v45, v45, v61
	v_fmac_f32_e32 v64, v69, v41
	v_add_f32_e32 v45, v60, v45
	v_add_f32_e32 v60, v62, v64
	v_sub_f32_e32 v63, v61, v60
	v_pk_add_f32 v[66:67], v[60:61], v[62:63] neg_lo:[0,1] neg_hi:[0,1]
	v_mov_b32_e32 v65, v60
	v_pk_add_f32 v[60:61], v[66:67], v[64:65] neg_lo:[0,1] neg_hi:[0,1]
	v_cmp_neq_f32_e32 vcc, s23, v37
	v_add_f32_e32 v45, v45, v61
	v_add_f32_e32 v45, v60, v45
	v_add_f32_e32 v61, v63, v45
	v_mul_f32_e32 v70, v68, v61
	v_mul_f32_e32 v62, v43, v70
	v_fma_f32 v64, v70, v43, -v62
	v_fmac_f32_e32 v64, v70, v41
	v_add_f32_e32 v60, v62, v64
	v_sub_f32_e32 v41, v63, v61
	v_sub_f32_e32 v63, v61, v60
	v_pk_add_f32 v[66:67], v[60:61], v[62:63] neg_lo:[0,1] neg_hi:[0,1]
	v_mov_b32_e32 v65, v60
	v_add_f32_e32 v41, v45, v41
	v_pk_add_f32 v[60:61], v[66:67], v[64:65] neg_lo:[0,1] neg_hi:[0,1]
	v_add_f32_e32 v43, v69, v70
	v_add_f32_e32 v41, v41, v61
	v_add_f32_e32 v41, v60, v41
	v_add_f32_e32 v41, v63, v41
	v_sub_f32_e32 v45, v43, v69
	v_mul_f32_e32 v41, v68, v41
	v_sub_f32_e32 v45, v70, v45
	v_add_f32_e32 v41, v45, v41
	v_add_f32_e32 v61, v43, v41
	v_cvt_f32_i32_e32 v60, v59
	v_mul_f32_e32 v62, v61, v61
	v_fmamk_f32 v45, v62, 0x3e9b6dac, v57
	v_fmaak_f32 v45, v62, v45, 0x3f2aaada
	v_sub_f32_e32 v43, v61, v43
	v_ldexp_f32 v63, v61, 1
	v_mul_f32_e32 v61, v61, v62
	v_pk_mul_f32 v[64:65], v[60:61], v[44:45]
	v_sub_f32_e32 v41, v41, v43
	v_fma_f32 v62, v60, s25, -v64
	v_fmac_f32_e32 v62, 0xb102e308, v60
	v_pk_add_f32 v[60:61], v[64:65], v[62:63]
	v_ldexp_f32 v41, v41, 1
	v_sub_f32_e32 v43, v61, v63
	v_sub_f32_e32 v43, v65, v43
	v_add_f32_e32 v67, v41, v43
	v_mov_b32_e32 v66, v64
	v_pk_add_f32 v[64:65], v[60:61], v[64:65] neg_lo:[0,1] neg_hi:[0,1]
	v_pk_add_f32 v[68:69], v[60:61], v[66:67]
	v_mov_b32_e32 v63, v60
	v_mov_b32_e32 v65, v69
	v_pk_add_f32 v[70:71], v[62:63], v[64:65] neg_lo:[0,1] neg_hi:[0,1]
	v_pk_add_f32 v[62:63], v[62:63], v[64:65]
	v_mov_b32_e32 v74, v61
	v_pk_add_f32 v[64:65], v[62:63], v[60:61] op_sel:[1,0] op_sel_hi:[0,1] neg_lo:[0,1] neg_hi:[0,1]
	v_pk_add_f32 v[72:73], v[68:69], v[64:65] op_sel_hi:[1,0] neg_lo:[0,1] neg_hi:[0,1]
	v_mov_b32_e32 v68, v69
	v_mov_b32_e32 v69, v63
	v_mov_b32_e32 v75, v64
	v_pk_add_f32 v[64:65], v[68:69], v[74:75] neg_lo:[0,1] neg_hi:[0,1]
	v_mov_b32_e32 v66, v67
	v_mov_b32_e32 v67, v60
	v_pk_add_f32 v[60:61], v[66:67], v[64:65] neg_lo:[0,1] neg_hi:[0,1]
	v_mov_b32_e32 v72, v70
	v_pk_add_f32 v[64:65], v[72:73], v[60:61]
	v_mov_b32_e32 v71, v63
	v_pk_add_f32 v[66:67], v[64:65], v[64:65] op_sel:[0,1] op_sel_hi:[1,0]
	s_nop 0
	v_pk_add_f32 v[62:63], v[62:63], v[66:67] op_sel:[1,0] op_sel_hi:[0,1]
	v_mov_b32_e32 v65, v62
	v_pk_add_f32 v[68:69], v[64:65], v[70:71] neg_lo:[0,1] neg_hi:[0,1]
	v_mov_b32_e32 v61, v66
	v_sub_f32_e32 v41, v64, v68
	v_pk_add_f32 v[60:61], v[60:61], v[68:69] neg_lo:[0,1] neg_hi:[0,1]
	v_sub_f32_e32 v41, v70, v41
	v_add_f32_e32 v41, v60, v41
	v_add_f32_e32 v41, v41, v61
	v_add_f32_e32 v41, v62, v41
	v_cndmask_b32_e32 v41, v58, v41, vcc
	v_cmp_gt_f32_e32 vcc, s26, v37
	s_nop 1
	v_cndmask_b32_e32 v37, v41, v37, vcc
	v_sub_f32_e32 v37, v39, v37
.Llsv_rk0_b:
	s_mov_b64 exec, s[98:99]
	s_nop 0
	v_mov_b32_e32 v230, v37
	s_branch .LBB0_987

.LBB0_1272:
	s_or_b64 exec, exec, s[4:5]
	s_mov_b32 s0, 0
	v_mov_b32_e32 v70, v0
	s_mov_b64 s[4:5], s[78:79]
	s_waitcnt lgkmcnt(0)
	s_barrier
	s_cmpk_gt_i32 s96, 0x7f
	v_writelane_b32 v232, s0, 41
	s_cselect_b64 s[2:3], -1, 0
	s_nop 0
	v_writelane_b32 v232, s1, 42
	v_readfirstlane_b32 s0, v70
	s_nop 1
	v_writelane_b32 v232, s0, 43
	v_writelane_b32 v232, s2, 44
	s_mov_b64 s[0:1], -1
	s_and_b64 vcc, exec, s[2:3]
	v_writelane_b32 v232, s3, 45
	v_writelane_b32 v232, s90, 46
	s_nop 1
	v_writelane_b32 v232, s91, 47
	v_writelane_b32 v232, s87, 48
	v_writelane_b32 v232, s95, 49
	v_writelane_b32 v232, s96, 51
	s_nop 1
	v_writelane_b32 v232, s97, 52
	s_cbranch_vccz .LBB0_1296
	v_writelane_b32 v232, s62, 53
	s_add_u32 s92, s4, 0x16400000
	v_writelane_b32 v232, s94, 54
	s_addc_u32 s93, s5, 0
	s_add_i32 s2, s96, 0xffffff80
	v_writelane_b32 v232, s95, 55
	s_add_i32 s6, s90, 0xffffff80
	s_mov_b32 s0, s2
	v_writelane_b32 v232, s0, 56
	s_cmpk_gt_u32 s2, 0x3ff
	v_readfirstlane_b32 s8, v70
	v_writelane_b32 v232, s1, 57
	s_cbranch_scc1 .LBB0_1286
	v_readlane_b32 s0, v232, 41
	v_readlane_b32 s1, v232, 42
	s_mov_b32 s2, s0
	s_lshl_b32 s0, s0, 4
	s_ashr_i32 s1, s0, 31
	v_readlane_b32 s12, v233, 0
	s_lshl_b64 s[0:1], s[0:1], 2
	v_readlane_b32 s22, v233, 10
	v_readlane_b32 s23, v233, 11
	s_add_u32 s78, s22, s0
	s_addc_u32 s79, s23, s1
	s_lshl_b32 s0, s2, 9
	s_ashr_i32 s1, s0, 31
	v_readlane_b32 s24, v233, 12
	s_lshl_b64 s[0:1], s[0:1], 2
	v_readlane_b32 s25, v233, 13
	s_add_u32 s0, s24, s0
	s_addc_u32 s1, s25, s1
	s_add_u32 s80, s4, 0x1a400000
	s_addc_u32 s81, s5, 0
	s_add_u32 s7, s4, 0x29400000
	v_readlane_b32 s2, v232, 51
	v_readlane_b32 s84, v232, 56
	s_addc_u32 s77, s5, 0
	s_and_b32 s2, s2, 31
	s_lshr_b32 s9, s84, 8
	s_lshl_b32 s10, s9, 12
	s_lshl_b32 s11, s2, 7
	v_readlane_b32 s3, v232, 52
	s_or_b32 s10, s10, s11
	s_bfe_u32 s3, s84, 0x30005
	s_mulk_i32 s10, 0x3400
	s_add_u32 s10, s80, s10
	s_addc_u32 s11, s81, 0
	s_lshl_b32 s12, s3, 7
	s_add_u32 s10, s10, s12
	s_addc_u32 s11, s11, 0
	s_lshl_b32 s9, s9, 4
	s_lshl_b32 s3, s3, 1
	s_or_b32 s3, s3, s9
	s_lshl_b32 s9, s3, 18
	s_lshl_b32 s12, s2, 13
	s_or_b32 s9, s9, s12
	v_readlane_b32 s13, v233, 1
	s_add_u32 s12, s7, s9
	s_addc_u32 s13, s77, 0
	s_lshl_b32 s3, s3, 5
	s_or_b32 s2, s3, s2
	v_readlane_b32 s14, v233, 2
	v_readlane_b32 s15, v233, 3
	s_mov_b32 s83, 0
	s_or_b32 s82, s2, 32
	s_lshl_b64 s[14:15], s[82:83], 13
	s_waitcnt vmcnt(0)
	v_lshlrev_b32_e32 v1, 3, v70
	v_lshlrev_b32_e32 v29, 2, v70
	v_add_u32_e32 v38, 0x200, v70
	s_add_u32 s14, s7, s14
	v_and_b32_e32 v26, 56, v1
	v_mov_b32_e32 v73, 0
	v_and_b32_e32 v28, 60, v29
	v_and_b32_e32 v16, 0xffffffc0, v29
	v_lshlrev_b32_e32 v36, 2, v38
	s_addc_u32 s15, s77, s15
	v_lshlrev_b32_e32 v72, 1, v26
	v_lshlrev_b32_e32 v30, 1, v28
	v_mov_b32_e32 v31, v73
	v_ashrrev_i32_e32 v17, 31, v16
	v_and_b32_e32 v36, 0xffffffc0, v36
	s_movk_i32 s90, 0x3400
	v_lshl_add_u64 v[14:15], s[10:11], 0, v[72:73]
	v_lshl_add_u64 v[32:33], s[12:13], 0, v[30:31]
	v_lshl_add_u64 v[34:35], s[14:15], 0, v[30:31]
	v_ashrrev_i32_e32 v31, 3, v70
	v_lshlrev_b64 v[76:77], 1, v[16:17]
	v_ashrrev_i32_e32 v37, 31, v36
	v_mad_i64_i32 v[10:11], s[10:11], v31, s90, v[14:15]
	v_lshl_add_u64 v[16:17], v[32:33], 0, v[76:77]
	v_ashrrev_i32_e32 v39, 3, v38
	v_lshlrev_b64 v[80:81], 1, v[36:37]
	global_load_dwordx4 v[2:5], v[10:11], off
	global_load_dwordx4 v[6:9], v[10:11], off offset:1024
	s_nop 0
	global_load_dwordx4 v[10:13], v[10:11], off offset:2048
	v_mad_i64_i32 v[22:23], s[10:11], v39, s90, v[14:15]
	global_load_dwordx2 v[94:95], v[16:17], off
	v_lshl_add_u64 v[16:17], v[34:35], 0, v[76:77]
	v_lshl_add_u64 v[32:33], v[32:33], 0, v[80:81]
	global_load_dwordx2 v[96:97], v[16:17], off
	s_nop 0
	global_load_dwordx4 v[14:17], v[22:23], off
	global_load_dwordx4 v[18:21], v[22:23], off offset:1024
	s_nop 0
	global_load_dwordx4 v[22:25], v[22:23], off offset:2048
	s_ashr_i32 s2, s8, 2
	global_load_dwordx2 v[98:99], v[32:33], off
	v_lshl_add_u64 v[32:33], v[34:35], 0, v[80:81]
	global_load_dwordx2 v[100:101], v[32:33], off
	v_bfi_b32 v82, -16, s2, v70
	s_movk_i32 s2, 0x90
	v_add_u32_e32 v34, 0, v30
	v_mul_lo_u32 v30, v82, s2
	v_add_u32_e32 v33, 0, v30
	v_lshrrev_b32_e32 v30, 2, v70
	v_and_b32_e32 v30, 12, v30
	v_sub_u32_e32 v41, 0x80, v82
	v_add_u32_e32 v32, 0, v72
	s_movk_i32 s3, 0x80
	v_cvt_f32_i32_e32 v71, v41
	v_bfrev_b32_e32 v41, 0.5
	v_lshlrev_b32_e32 v72, 2, v30
	v_mad_i64_i32 v[74:75], s[10:11], v31, s90, 0
	v_and_b32_e32 v35, 48, v70
	v_bitop3_b32 v116, v29, 64, v41 bitop3:0x6c
	v_bitop3_b32 v117, v29, s3, v41 bitop3:0x6c
	v_lshl_add_u64 v[84:85], s[0:1], 0, v[72:73]
	v_mad_u64_u32 v[86:87], s[0:1], v31, s2, v[32:33]
	v_lshrrev_b32_e32 v29, 4, v70
	v_sub_u32_e32 v31, v82, v30
	v_mad_u64_u32 v[88:89], s[0:1], v29, s2, v[34:35]
	v_cvt_f32_i32_e32 v87, v31
	v_sub_u32_e32 v31, v30, v82
	v_lshrrev_b32_e32 v29, 4, v38
	v_cvt_f32_i32_e32 v89, v31
	v_or_b32_e32 v31, 1, v30
	v_mad_u64_u32 v[90:91], s[0:1], v39, s2, v[32:33]
	v_mad_u64_u32 v[92:93], s[0:1], v29, s2, v[34:35]
	v_sub_u32_e32 v32, v31, v82
	v_sub_u32_e32 v31, v82, v31
	v_cvt_f32_i32_e32 v93, v31
	v_or_b32_e32 v31, 2, v30
	v_cvt_f32_i32_e32 v91, v32
	v_cmp_gt_i32_e64 s[12:13], v31, v82
	v_sub_u32_e32 v32, v82, v31
	v_sub_u32_e32 v31, v31, v82
	v_cvt_f32_i32_e32 v119, v31
	v_or_b32_e32 v31, 3, v30
	v_cvt_f32_i32_e32 v118, v32
	v_cmp_gt_i32_e64 s[14:15], v31, v82
	v_sub_u32_e32 v32, v82, v31
	v_sub_u32_e32 v31, v31, v82
	v_readlane_b32 s16, v233, 4
	v_readlane_b32 s17, v233, 5
	v_cvt_f32_i32_e32 v121, v31
	v_or_b32_e32 v31, 16, v30
	v_cvt_f32_i32_e32 v120, v32
	v_cmp_gt_i32_e64 s[16:17], v31, v82
	v_sub_u32_e32 v32, v82, v31
	v_sub_u32_e32 v31, v31, v82
	v_readlane_b32 s18, v233, 6
	v_readlane_b32 s19, v233, 7
	v_cvt_f32_i32_e32 v123, v31
	v_or_b32_e32 v31, 17, v30
	v_cvt_f32_i32_e32 v122, v32
	v_cmp_gt_i32_e64 s[18:19], v31, v82
	v_sub_u32_e32 v32, v82, v31
	v_sub_u32_e32 v31, v31, v82
	v_readlane_b32 s20, v233, 8
	v_readlane_b32 s21, v233, 9
	v_cvt_f32_i32_e32 v125, v31
	v_or_b32_e32 v31, 18, v30
	v_cvt_f32_i32_e32 v124, v32
	v_cmp_gt_i32_e64 s[20:21], v31, v82
	v_sub_u32_e32 v32, v82, v31
	v_sub_u32_e32 v31, v31, v82
	v_cvt_f32_i32_e32 v127, v31
	v_or_b32_e32 v31, 19, v30
	v_cvt_f32_i32_e32 v126, v32
	v_cmp_gt_i32_e64 s[22:23], v31, v82
	v_sub_u32_e32 v32, v82, v31
	v_sub_u32_e32 v31, v31, v82
	v_cvt_f32_i32_e32 v129, v31
	v_or_b32_e32 v31, 32, v30
	v_cvt_f32_i32_e32 v128, v32
	v_sub_u32_e32 v32, v82, v31
	v_cvt_f32_i32_e32 v130, v32
	v_sub_u32_e32 v32, v31, v82
	v_readlane_b32 s26, v233, 14
	v_readlane_b32 s27, v233, 15
	v_cvt_f32_i32_e32 v131, v32
	v_or_b32_e32 v32, 33, v30
	v_cmp_gt_i32_e64 s[26:27], v32, v82
	v_sub_u32_e32 v34, v82, v32
	v_sub_u32_e32 v32, v32, v82
	v_cvt_f32_i32_e32 v133, v32
	v_or_b32_e32 v32, 34, v30
	v_cvt_f32_i32_e32 v132, v34
	v_cmp_gt_i32_e64 s[28:29], v32, v82
	v_sub_u32_e32 v34, v82, v32
	v_sub_u32_e32 v32, v32, v82
	v_cvt_f32_i32_e32 v135, v32
	v_or_b32_e32 v32, 35, v30
	v_cvt_f32_i32_e32 v134, v34
	v_cmp_gt_i32_e64 s[30:31], v32, v82
	v_sub_u32_e32 v34, v82, v32
	v_sub_u32_e32 v32, v32, v82
	v_cvt_f32_i32_e32 v137, v32
	v_or_b32_e32 v32, 48, v30
	v_cvt_f32_i32_e32 v136, v34
	v_cmp_gt_i32_e64 s[34:35], v32, v82
	v_sub_u32_e32 v34, v82, v32
	v_sub_u32_e32 v32, v32, v82
	v_cvt_f32_i32_e32 v139, v32
	v_or_b32_e32 v32, 49, v30
	v_cvt_f32_i32_e32 v138, v34
	v_cmp_gt_i32_e64 s[36:37], v32, v82
	v_sub_u32_e32 v34, v82, v32
	v_sub_u32_e32 v32, v32, v82
	v_cvt_f32_i32_e32 v141, v32
	v_or_b32_e32 v32, 50, v30
	v_cvt_f32_i32_e32 v140, v34
	v_cmp_gt_i32_e64 s[38:39], v32, v82
	v_sub_u32_e32 v34, v82, v32
	v_sub_u32_e32 v32, v32, v82
	v_cvt_f32_i32_e32 v143, v32
	v_or_b32_e32 v32, 51, v30
	v_cvt_f32_i32_e32 v142, v34
	v_cmp_gt_i32_e64 s[40:41], v32, v82
	v_sub_u32_e32 v34, v82, v32
	v_sub_u32_e32 v32, v32, v82
	v_cvt_f32_i32_e32 v145, v32
	v_or_b32_e32 v32, 64, v30
	v_cvt_f32_i32_e32 v144, v34
	v_sub_u32_e32 v34, v82, v32
	v_cvt_f32_i32_e32 v146, v34
	v_sub_u32_e32 v34, v32, v82
	v_cvt_f32_i32_e32 v147, v34
	v_or_b32_e32 v34, 0x41, v30
	v_cmp_gt_i32_e64 s[44:45], v34, v82
	v_sub_u32_e32 v38, v82, v34
	v_sub_u32_e32 v34, v34, v82
	v_cvt_f32_i32_e32 v149, v34
	v_or_b32_e32 v34, 0x42, v30
	v_cvt_f32_i32_e32 v148, v38
	v_cmp_gt_i32_e64 s[46:47], v34, v82
	v_sub_u32_e32 v38, v82, v34
	v_sub_u32_e32 v34, v34, v82
	v_cvt_f32_i32_e32 v151, v34
	v_or_b32_e32 v34, 0x43, v30
	v_cvt_f32_i32_e32 v150, v38
	v_cmp_gt_i32_e64 s[48:49], v34, v82
	v_sub_u32_e32 v38, v82, v34
	v_sub_u32_e32 v34, v34, v82
	v_cvt_f32_i32_e32 v153, v34
	v_or_b32_e32 v34, 0x50, v30
	v_cvt_f32_i32_e32 v152, v38
	v_cmp_gt_i32_e64 s[50:51], v34, v82
	v_sub_u32_e32 v38, v82, v34
	v_sub_u32_e32 v34, v34, v82
	v_cvt_f32_i32_e32 v155, v34
	v_or_b32_e32 v34, 0x51, v30
	v_cvt_f32_i32_e32 v154, v38
	v_cmp_gt_i32_e64 s[52:53], v34, v82
	v_sub_u32_e32 v38, v82, v34
	v_sub_u32_e32 v34, v34, v82
	v_cvt_f32_i32_e32 v157, v34
	v_or_b32_e32 v34, 0x52, v30
	v_cvt_f32_i32_e32 v156, v38
	v_cmp_gt_i32_e64 s[54:55], v34, v82
	v_sub_u32_e32 v38, v82, v34
	v_sub_u32_e32 v34, v34, v82
	v_cvt_f32_i32_e32 v159, v34
	v_or_b32_e32 v34, 0x53, v30
	v_cvt_f32_i32_e32 v158, v38
	v_cmp_gt_i32_e64 s[94:95], v34, v82
	v_sub_u32_e32 v38, v82, v34
	v_sub_u32_e32 v34, v34, v82
	v_cvt_f32_i32_e32 v161, v34
	v_or_b32_e32 v34, 0x60, v30
	v_cvt_f32_i32_e32 v160, v38
	v_sub_u32_e32 v38, v82, v34
	v_cvt_f32_i32_e32 v162, v38
	v_sub_u32_e32 v38, v34, v82
	v_cvt_f32_i32_e32 v163, v38
	v_or_b32_e32 v38, 0x61, v30
	v_mad_i64_i32 v[78:79], s[10:11], v39, s90, 0
	v_cmp_gt_i32_e64 s[60:61], v38, v82
	v_sub_u32_e32 v39, v82, v38
	v_sub_u32_e32 v38, v38, v82
	v_cvt_f32_i32_e32 v165, v38
	v_or_b32_e32 v38, 0x62, v30
	v_cvt_f32_i32_e32 v164, v39
	v_cmp_gt_i32_e64 s[62:63], v38, v82
	v_sub_u32_e32 v39, v82, v38
	v_sub_u32_e32 v38, v38, v82
	v_cvt_f32_i32_e32 v167, v38
	v_or_b32_e32 v38, 0x63, v30
	v_cvt_f32_i32_e32 v166, v39
	v_cmp_gt_i32_e64 s[64:65], v38, v82
	v_sub_u32_e32 v39, v82, v38
	v_sub_u32_e32 v38, v38, v82
	v_cvt_f32_i32_e32 v169, v38
	v_or_b32_e32 v38, 0x70, v30
	v_cvt_f32_i32_e32 v168, v39
	v_cmp_gt_i32_e64 s[66:67], v38, v82
	v_sub_u32_e32 v39, v82, v38
	v_sub_u32_e32 v38, v38, v82
	v_cvt_f32_i32_e32 v171, v38
	v_or_b32_e32 v38, 0x71, v30
	v_cvt_f32_i32_e32 v170, v39
	v_cmp_gt_i32_e64 s[68:69], v38, v82
	v_sub_u32_e32 v39, v82, v38
	v_sub_u32_e32 v38, v38, v82
	v_cvt_f32_i32_e32 v173, v38
	v_or_b32_e32 v38, 0x72, v30
	v_cvt_f32_i32_e32 v172, v39
	v_cmp_gt_i32_e64 s[70:71], v38, v82
	v_sub_u32_e32 v39, v82, v38
	v_sub_u32_e32 v38, v38, v82
	v_and_b32_e32 v1, 24, v1
	v_cvt_f32_i32_e32 v175, v38
	v_or_b32_e32 v38, 0x73, v30
	v_add_u32_e32 v40, 0, v1
	v_add_u32_e32 v1, 1, v82
	v_cvt_f32_i32_e32 v174, v39
	v_cmp_gt_i32_e64 s[72:73], v38, v82
	v_sub_u32_e32 v39, v82, v38
	v_sub_u32_e32 v38, v38, v82
	v_and_b32_e32 v27, 15, v70
	v_bfe_u32 v37, v70, 2, 2
	v_cvt_f32_i32_e32 v1, v1
	v_cvt_f32_i32_e32 v176, v39
	v_cvt_f32_i32_e32 v177, v38
	v_add_u32_e32 v36, 0, v35
	v_mul_u32_u24_e32 v29, 0x90, v27
	v_cmp_gt_i32_e64 s[24:25], v31, v82
	v_cmp_gt_i32_e64 s[42:43], v32, v82
	v_cmp_gt_i32_e64 s[58:59], v34, v82
	v_or_b32_e32 v38, v30, v37
	v_or_b32_e32 v31, v31, v37
	v_or_b32_e32 v32, v32, v37
	v_or_b32_e32 v34, v34, v37
	v_mul_u32_u24_e32 v27, 0x48, v27
	v_mul_u32_u24_e32 v38, 0x90, v38
	v_mul_u32_u24_e32 v31, 0x90, v31
	v_mul_u32_u24_e32 v32, 0x90, v32
	v_mul_u32_u24_e32 v34, 0x90, v34
	v_lshl_add_u32 v178, v27, 1, v36
	v_ashrrev_i32_e32 v83, 31, v82
	v_cmp_gt_i32_e64 s[8:9], v30, v82
	v_cmp_lt_i32_e64 s[10:11], v30, v82
	v_add_u32_e32 v179, 0x900, v178
	v_add_u32_e32 v180, 0x1200, v178
	v_add_u32_e32 v181, 0x1b00, v178
	s_mov_b32 s91, 0xbfb8aa3b
	s_mov_b32 s89, 0x42ce8ed0
	s_mov_b32 s88, 0xc2b17218
	s_mov_b32 s56, 0x7f800000
	s_mov_b32 s76, 0x3f2aaaab
	v_mov_b32_e32 v182, 0x3ecc95a3
	s_mov_b32 s74, 0x3f317218
	s_mov_b32 s75, 0x33800000
	s_mov_b32 s57, 0x3fb8aa3b
	v_lshlrev_b32_e32 v102, 1, v26
	v_lshlrev_b32_e32 v104, 1, v28
	v_add_u32_e32 v183, v33, v35
	v_add_u32_e32 v184, v36, v29
	v_add_u32_e32 v185, v40, v38
	v_add_u32_e32 v186, v40, v31
	v_add_u32_e32 v187, v40, v32
	v_add_u32_e32 v188, v40, v34
	v_lshlrev_b32_e32 v72, 1, v30
	v_mov_b32_e32 v189, 0x3a27c5ac
	v_mov_b32_e32 v190, 0x260
	v_mov_b32_e32 v191, 0x7f800000
	v_mov_b32_e32 v106, 0x3f317218
	s_mov_b32 s82, s84
	v_readlane_b32 s85, v232, 57
	v_mbcnt_lo_u32_b32 v221, -1, 0
	v_mbcnt_hi_u32_b32 v221, -1, v221
	v_and_b32_e32 v221, 15, v221
	v_lshlrev_b32_e32 v26, 2, v221
	global_load_dword v26, v26, s[78:79]
	s_waitcnt vmcnt(0)
	v_cmp_ngt_f32_e32 vcc, 0, v26
	s_and_saveexec_b64 s[98:99], vcc
	s_cbranch_execz .Llsv_ro0_a
	v_mul_f32_e32 v27, 0xbfb8aa3b, v26
	v_rndne_f32_e32 v28, v27
	v_sub_f32_e32 v29, v27, v28
	v_fma_f32 v27, v26, s91, -v27
	v_fmac_f32_e32 v27, 0xb2a5705f, v26
	v_add_f32_e32 v27, v29, v27
	v_cvt_i32_f32_e32 v28, v28
	v_exp_f32_e32 v27, v27
	v_cmp_nlt_f32_e32 vcc, s89, v26
	v_ldexp_f32 v27, v27, v28
	s_nop 0
	v_cndmask_b32_e32 v27, 0, v27, vcc
	v_cmp_ngt_f32_e32 vcc, s88, v26
	s_nop 1
	v_cndmask_b32_e32 v27, v191, v27, vcc
	v_add_f32_e32 v30, 1.0, v27
	v_add_f32_e32 v28, -1.0, v30
	v_sub_f32_e32 v29, v28, v30
	v_add_f32_e32 v29, 1.0, v29
	v_sub_f32_e32 v28, v27, v28
	v_add_f32_e32 v31, v28, v29
	v_frexp_mant_f32_e32 v32, v30
	v_cvt_f64_f32_e32 v[28:29], v30
	v_frexp_exp_i32_f64_e32 v28, v[28:29]
	v_cmp_gt_f32_e32 vcc, s76, v32
	s_nop 1
	v_subbrev_co_u32_e32 v36, vcc, 0, v28, vcc
	v_sub_u32_e32 v28, 0, v36
	v_ldexp_f32 v29, v30, v28
	v_add_f32_e32 v30, -1.0, v29
	v_add_f32_e32 v32, 1.0, v29
	v_ldexp_f32 v28, v31, v28
	v_add_f32_e32 v31, 1.0, v30
	v_add_f32_e32 v33, -1.0, v32
	v_sub_f32_e32 v31, v29, v31
	v_sub_f32_e32 v29, v29, v33
	v_add_f32_e32 v31, v28, v31
	v_add_f32_e32 v28, v28, v29
	v_add_f32_e32 v37, v32, v28
	v_rcp_f32_e32 v39, v37
	v_sub_f32_e32 v29, v32, v37
	v_add_f32_e32 v38, v28, v29
	v_add_f32_e32 v29, v30, v31
	v_mul_f32_e32 v41, v29, v39
	v_sub_f32_e32 v28, v30, v29
	v_mul_f32_e32 v30, v37, v41
	v_fma_f32 v32, v41, v37, -v30
	v_fmac_f32_e32 v32, v41, v38
	v_add_f32_e32 v40, v31, v28
	v_add_f32_e32 v28, v30, v32
	v_sub_f32_e32 v31, v29, v28
	v_pk_add_f32 v[34:35], v[28:29], v[30:31] neg_lo:[0,1] neg_hi:[0,1]
	v_mov_b32_e32 v33, v28
	v_pk_add_f32 v[28:29], v[34:35], v[32:33] neg_lo:[0,1] neg_hi:[0,1]
	v_cmp_neq_f32_e32 vcc, s56, v27
	v_add_f32_e32 v29, v40, v29
	v_add_f32_e32 v28, v28, v29
	v_add_f32_e32 v29, v31, v28
	v_mul_f32_e32 v40, v39, v29
	v_mul_f32_e32 v30, v37, v40
	v_fma_f32 v32, v40, v37, -v30
	v_fmac_f32_e32 v32, v40, v38
	v_sub_f32_e32 v31, v31, v29
	v_add_f32_e32 v37, v28, v31
	v_add_f32_e32 v28, v30, v32
	v_sub_f32_e32 v31, v29, v28
	v_pk_add_f32 v[34:35], v[28:29], v[30:31] neg_lo:[0,1] neg_hi:[0,1]
	v_mov_b32_e32 v33, v28
	v_pk_add_f32 v[28:29], v[34:35], v[32:33] neg_lo:[0,1] neg_hi:[0,1]
	s_nop 0
	v_add_f32_e32 v29, v37, v29
	v_add_f32_e32 v28, v28, v29
	v_add_f32_e32 v29, v41, v40
	v_add_f32_e32 v28, v31, v28
	v_sub_f32_e32 v30, v29, v41
	v_mul_f32_e32 v28, v39, v28
	v_sub_f32_e32 v30, v40, v30
	v_add_f32_e32 v30, v30, v28
	v_add_f32_e32 v32, v29, v30
	v_mul_f32_e32 v33, v32, v32
	v_fmamk_f32 v28, v33, 0x3e9b6dac, v182
	v_fmaak_f32 v107, v33, v28, 0x3f2aaada
	v_cvt_f32_i32_e32 v28, v36
	v_sub_f32_e32 v29, v32, v29
	v_sub_f32_e32 v29, v30, v29
	v_ldexp_f32 v34, v29, 1
	v_mul_f32_e32 v29, v32, v33
	v_ldexp_f32 v31, v32, 1
	v_pk_mul_f32 v[32:33], v[28:29], v[106:107]
	s_nop 0
	v_fma_f32 v30, v28, s74, -v32
	v_fmac_f32_e32 v30, 0xb102e308, v28
	v_pk_add_f32 v[28:29], v[32:33], v[30:31]
	s_nop 0
	v_sub_f32_e32 v31, v29, v31
	v_sub_f32_e32 v31, v33, v31
	v_add_f32_e32 v35, v34, v31
	v_mov_b32_e32 v34, v32
	v_pk_add_f32 v[32:33], v[28:29], v[32:33] neg_lo:[0,1] neg_hi:[0,1]
	v_pk_add_f32 v[36:37], v[28:29], v[34:35]
	v_mov_b32_e32 v31, v28
	v_mov_b32_e32 v33, v37
	v_pk_add_f32 v[38:39], v[30:31], v[32:33] neg_lo:[0,1] neg_hi:[0,1]
	v_pk_add_f32 v[30:31], v[30:31], v[32:33]
	v_mov_b32_e32 v42, v29
	v_pk_add_f32 v[32:33], v[30:31], v[28:29] op_sel:[1,0] op_sel_hi:[0,1] neg_lo:[0,1] neg_hi:[0,1]
	v_pk_add_f32 v[40:41], v[36:37], v[32:33] op_sel_hi:[1,0] neg_lo:[0,1] neg_hi:[0,1]
	v_mov_b32_e32 v36, v37
	v_mov_b32_e32 v37, v31
	v_mov_b32_e32 v43, v32
	v_pk_add_f32 v[32:33], v[36:37], v[42:43] neg_lo:[0,1] neg_hi:[0,1]
	v_mov_b32_e32 v34, v35
	v_mov_b32_e32 v35, v28
	v_pk_add_f32 v[28:29], v[34:35], v[32:33] neg_lo:[0,1] neg_hi:[0,1]
	v_mov_b32_e32 v40, v38
	v_pk_add_f32 v[32:33], v[40:41], v[28:29]
	v_mov_b32_e32 v39, v31
	v_pk_add_f32 v[34:35], v[32:33], v[32:33] op_sel:[0,1] op_sel_hi:[1,0]
	s_nop 0
	v_pk_add_f32 v[30:31], v[30:31], v[34:35] op_sel:[1,0] op_sel_hi:[0,1]
	v_mov_b32_e32 v33, v30
	v_pk_add_f32 v[36:37], v[32:33], v[38:39] neg_lo:[0,1] neg_hi:[0,1]
	v_mov_b32_e32 v29, v34
	v_sub_f32_e32 v31, v32, v36
	v_pk_add_f32 v[28:29], v[28:29], v[36:37] neg_lo:[0,1] neg_hi:[0,1]
	v_sub_f32_e32 v31, v38, v31
	v_add_f32_e32 v28, v28, v31
	v_add_f32_e32 v28, v28, v29
	v_add_f32_e32 v28, v30, v28
	v_cndmask_b32_e32 v28, v191, v28, vcc
	v_cmp_lt_f32_e64 vcc, |v27|, s75
	s_nop 1
	v_cndmask_b32_e32 v27, v28, v27, vcc
	v_xor_b32_e32 v108, 0x80000000, v27
.Llsv_ro0_a:
	s_xor_b64 exec, exec, s[98:99]
	s_cbranch_execz .Llsv_ro0_b
	v_mul_f32_e32 v27, 0x3fb8aa3b, v26
	v_rndne_f32_e32 v28, v27
	v_sub_f32_e32 v29, v27, v28
	v_fma_f32 v27, v26, s57, -v27
	v_fmac_f32_e32 v27, 0x32a5705f, v26
	v_add_f32_e32 v27, v29, v27
	v_cvt_i32_f32_e32 v28, v28
	v_exp_f32_e32 v27, v27
	s_mov_b32 s2, 0xc2ce8ed0
	v_cmp_ngt_f32_e32 vcc, s2, v26
	s_mov_b32 s2, 0x42b17218
	v_ldexp_f32 v27, v27, v28
	v_cndmask_b32_e32 v27, 0, v27, vcc
	v_cmp_nlt_f32_e32 vcc, s2, v26
	s_nop 1
	v_cndmask_b32_e32 v27, v191, v27, vcc
	v_add_f32_e32 v30, 1.0, v27
	v_add_f32_e32 v28, -1.0, v30
	v_sub_f32_e32 v29, v28, v30
	v_add_f32_e32 v29, 1.0, v29
	v_sub_f32_e32 v28, v27, v28
	v_add_f32_e32 v31, v28, v29
	v_frexp_mant_f32_e32 v32, v30
	v_cvt_f64_f32_e32 v[28:29], v30
	v_frexp_exp_i32_f64_e32 v28, v[28:29]
	v_cmp_gt_f32_e32 vcc, s76, v32
	s_nop 1
	v_subbrev_co_u32_e32 v36, vcc, 0, v28, vcc
	v_sub_u32_e32 v28, 0, v36
	v_ldexp_f32 v29, v30, v28
	v_add_f32_e32 v30, -1.0, v29
	v_add_f32_e32 v32, 1.0, v29
	v_ldexp_f32 v28, v31, v28
	v_add_f32_e32 v31, 1.0, v30
	v_add_f32_e32 v33, -1.0, v32
	v_sub_f32_e32 v31, v29, v31
	v_sub_f32_e32 v29, v29, v33
	v_add_f32_e32 v31, v28, v31
	v_add_f32_e32 v28, v28, v29
	v_add_f32_e32 v37, v32, v28
	v_rcp_f32_e32 v39, v37
	v_sub_f32_e32 v29, v32, v37
	v_add_f32_e32 v38, v28, v29
	v_add_f32_e32 v29, v30, v31
	v_mul_f32_e32 v41, v29, v39
	v_sub_f32_e32 v28, v30, v29
	v_mul_f32_e32 v30, v37, v41
	v_fma_f32 v32, v41, v37, -v30
	v_fmac_f32_e32 v32, v41, v38
	v_add_f32_e32 v40, v31, v28
	v_add_f32_e32 v28, v30, v32
	v_sub_f32_e32 v31, v29, v28
	v_pk_add_f32 v[34:35], v[28:29], v[30:31] neg_lo:[0,1] neg_hi:[0,1]
	v_mov_b32_e32 v33, v28
	v_pk_add_f32 v[28:29], v[34:35], v[32:33] neg_lo:[0,1] neg_hi:[0,1]
	v_cmp_neq_f32_e32 vcc, s56, v27
	v_add_f32_e32 v29, v40, v29
	v_add_f32_e32 v28, v28, v29
	v_add_f32_e32 v29, v31, v28
	v_mul_f32_e32 v40, v39, v29
	v_mul_f32_e32 v30, v37, v40
	v_fma_f32 v32, v40, v37, -v30
	v_fmac_f32_e32 v32, v40, v38
	v_sub_f32_e32 v31, v31, v29
	v_add_f32_e32 v37, v28, v31
	v_add_f32_e32 v28, v30, v32
	v_sub_f32_e32 v31, v29, v28
	v_pk_add_f32 v[34:35], v[28:29], v[30:31] neg_lo:[0,1] neg_hi:[0,1]
	v_mov_b32_e32 v33, v28
	v_pk_add_f32 v[28:29], v[34:35], v[32:33] neg_lo:[0,1] neg_hi:[0,1]
	s_nop 0
	v_add_f32_e32 v29, v37, v29
	v_add_f32_e32 v28, v28, v29
	v_add_f32_e32 v29, v41, v40
	v_add_f32_e32 v28, v31, v28
	v_sub_f32_e32 v30, v29, v41
	v_mul_f32_e32 v28, v39, v28
	v_sub_f32_e32 v30, v40, v30
	v_add_f32_e32 v30, v30, v28
	v_add_f32_e32 v32, v29, v30
	v_mul_f32_e32 v33, v32, v32
	v_fmamk_f32 v28, v33, 0x3e9b6dac, v182
	v_fmaak_f32 v107, v33, v28, 0x3f2aaada
	v_cvt_f32_i32_e32 v28, v36
	v_sub_f32_e32 v29, v32, v29
	v_sub_f32_e32 v29, v30, v29
	v_ldexp_f32 v34, v29, 1
	v_mul_f32_e32 v29, v32, v33
	v_ldexp_f32 v31, v32, 1
	v_pk_mul_f32 v[32:33], v[28:29], v[106:107]
	s_nop 0
	v_fma_f32 v30, v28, s74, -v32
	v_fmac_f32_e32 v30, 0xb102e308, v28
	v_pk_add_f32 v[28:29], v[32:33], v[30:31]
	s_nop 0
	v_sub_f32_e32 v31, v29, v31
	v_sub_f32_e32 v31, v33, v31
	v_add_f32_e32 v35, v34, v31
	v_mov_b32_e32 v34, v32
	v_pk_add_f32 v[32:33], v[28:29], v[32:33] neg_lo:[0,1] neg_hi:[0,1]
	v_pk_add_f32 v[36:37], v[28:29], v[34:35]
	v_mov_b32_e32 v31, v28
	v_mov_b32_e32 v33, v37
	v_pk_add_f32 v[38:39], v[30:31], v[32:33] neg_lo:[0,1] neg_hi:[0,1]
	v_pk_add_f32 v[30:31], v[30:31], v[32:33]
	v_mov_b32_e32 v42, v29
	v_pk_add_f32 v[32:33], v[30:31], v[28:29] op_sel:[1,0] op_sel_hi:[0,1] neg_lo:[0,1] neg_hi:[0,1]
	v_pk_add_f32 v[40:41], v[36:37], v[32:33] op_sel_hi:[1,0] neg_lo:[0,1] neg_hi:[0,1]
	v_mov_b32_e32 v36, v37
	v_mov_b32_e32 v37, v31
	v_mov_b32_e32 v43, v32
	v_pk_add_f32 v[32:33], v[36:37], v[42:43] neg_lo:[0,1] neg_hi:[0,1]
	v_mov_b32_e32 v34, v35
	v_mov_b32_e32 v35, v28
	v_pk_add_f32 v[28:29], v[34:35], v[32:33] neg_lo:[0,1] neg_hi:[0,1]
	v_mov_b32_e32 v40, v38
	v_pk_add_f32 v[32:33], v[40:41], v[28:29]
	v_mov_b32_e32 v39, v31
	v_pk_add_f32 v[34:35], v[32:33], v[32:33] op_sel:[0,1] op_sel_hi:[1,0]
	s_nop 0
	v_pk_add_f32 v[30:31], v[30:31], v[34:35] op_sel:[1,0] op_sel_hi:[0,1]
	v_mov_b32_e32 v33, v30
	v_pk_add_f32 v[36:37], v[32:33], v[38:39] neg_lo:[0,1] neg_hi:[0,1]
	v_mov_b32_e32 v29, v34
	v_sub_f32_e32 v31, v32, v36
	v_pk_add_f32 v[28:29], v[28:29], v[36:37] neg_lo:[0,1] neg_hi:[0,1]
	v_sub_f32_e32 v31, v38, v31
	v_add_f32_e32 v28, v28, v31
	v_add_f32_e32 v28, v28, v29
	v_add_f32_e32 v28, v30, v28
	v_cndmask_b32_e32 v28, v191, v28, vcc
	v_cmp_gt_f32_e32 vcc, s75, v27
	s_nop 1
	v_cndmask_b32_e32 v27, v28, v27, vcc
	v_sub_f32_e32 v108, v26, v27
.Llsv_ro0_b:
	s_mov_b64 exec, s[98:99]
	s_nop 0
	v_mov_b32_e32 v222, v108
	s_branch .LBB0_1276

.LBB0_1276:
	s_ashr_i32 s86, s82, 31
	s_lshr_b32 s0, s86, 27
	s_add_i32 s0, s82, s0
	s_ashr_i32 s87, s0, 5
	s_and_b32 s97, s87, 7
	s_lshl_b32 s0, s97, 2
	v_mov_b32_e32 v26, s0
	s_add_u32 s0, s78, s0
	s_addc_u32 s1, s79, 0
	s_waitcnt vmcnt(0)
	v_readlane_b32 vcc_lo, v222, s97
	s_add_i32 vcc_hi, s97, 8
	s_nop 1
	v_mov_b32_e32 v108, vcc_lo
	v_readlane_b32 vcc_lo, v222, vcc_hi
	s_nop 1
	v_mov_b32_e32 v107, vcc_lo

.LBB0_3302:
	s_andn2_b64 vcc, exec, s[12:13]
	s_cbranch_vccnz .LBB0_3316
	v_readlane_b32 s12, v233, 0
	s_lshl_b32 s2, s6, 4
	v_readlane_b32 s16, v233, 4
	v_readlane_b32 s17, v233, 5
	v_readlane_b32 s18, v233, 6
	v_readlane_b32 s19, v233, 7
	v_readlane_b32 s20, v233, 8
	v_readlane_b32 s21, v233, 9
	s_ashr_i32 s3, s2, 31
	v_readlane_b32 s22, v233, 10
	v_readlane_b32 s23, v233, 11
	v_readlane_b32 s24, v233, 12
	v_readlane_b32 s25, v233, 13
	s_mov_b64 s[16:17], s[20:21]
	s_ashr_i32 s7, s10, 8
	s_lshl_b64 s[2:3], s[2:3], 2
	s_mov_b64 s[18:19], s[22:23]
	v_readlane_b32 s13, v233, 1
	s_add_u32 s12, s18, s2
	s_addc_u32 s13, s19, s3
	s_add_u32 s8, s4, 0x27400000
	s_addc_u32 s9, s5, 0
	s_lshl_b32 s60, s96, 1
	v_readlane_b32 s15, v233, 3
	s_add_i32 s3, s7, s60
	v_readlane_b32 s14, v233, 2
	s_mul_i32 s2, s7, 0xd800
	s_bfe_u32 s15, s10, 0x20006
	s_ashr_i32 s10, s3, 31
	s_add_i32 s14, s2, 0
	s_lshr_b32 s2, s10, 27
	s_add_i32 s16, s3, s2
	s_and_b32 s2, s16, 0xffffffe0
	s_lshr_b32 s10, s10, 24
	s_sub_i32 s2, s3, s2
	s_add_i32 s3, s3, s10
	s_ashr_i32 s10, s3, 8
	s_ashr_i32 s11, s10, 31
	s_ashr_i32 s3, s2, 31
	s_lshl_b64 s[10:11], s[10:11], 12
	s_lshl_b64 s[2:3], s[2:3], 7
	s_add_u32 s2, s10, s2
	s_addc_u32 s3, s11, s3
	s_mulk_i32 s3, 0x3400
	s_mul_hi_u32 s10, s2, 0x3400
	s_add_i32 s10, s10, s3
	s_mulk_i32 s2, 0x3400
	s_add_u32 s2, s0, s2
	s_addc_u32 s3, s1, s10
	s_lshl_b32 s10, s16, 2
	s_and_b32 s10, s10, 0x380
	s_waitcnt vmcnt(0)
	v_bfe_u32 v37, v1, 3, 5
	s_add_u32 s2, s2, s10
	v_mul_u32_u24_e32 v36, 0x1a00, v37
	s_addc_u32 s3, s3, 0
	v_and_b32_e32 v38, 56, v119
	v_mov_b32_e32 v35, 0
	v_lshlrev_b32_e32 v34, 1, v36
	v_lshl_add_u64 v[2:3], s[2:3], 0, v[34:35]
	v_lshlrev_b32_e32 v34, 1, v38
	v_lshl_add_u64 v[26:27], v[2:3], 0, v[34:35]
	s_mov_b32 s2, 0x68000
	v_add_co_u32_e32 v14, vcc, s2, v26
	s_mov_b32 s2, 0xd0000
	s_nop 0
	v_addc_co_u32_e32 v15, vcc, 0, v27, vcc
	v_add_co_u32_e32 v22, vcc, s2, v26
	s_mov_b32 s2, 0x138000
	s_nop 0
	v_addc_co_u32_e32 v23, vcc, 0, v27, vcc
	v_add_co_u32_e32 v30, vcc, s2, v26
	global_load_dwordx4 v[2:5], v[26:27], off offset:1024
	global_load_dwordx4 v[6:9], v[26:27], off offset:2048
	v_addc_co_u32_e32 v31, vcc, 0, v27, vcc
	global_load_dwordx4 v[10:13], v[14:15], off offset:1024
	s_nop 0
	global_load_dwordx4 v[14:17], v[14:15], off offset:2048
	s_nop 0
	global_load_dwordx4 v[18:21], v[22:23], off offset:1024
	s_nop 0
	global_load_dwordx4 v[22:25], v[22:23], off offset:2048
	s_nop 0
	global_load_dwordx4 v[26:29], v[30:31], off offset:1024
	s_nop 0
	global_load_dwordx4 v[30:33], v[30:31], off offset:2048
	v_lshrrev_b32_e32 v39, 3, v1
	v_lshlrev_b32_e32 v43, 6, v111
	s_movk_i32 s3, 0x7f
	v_lshl_or_b32 v44, s15, 10, v43
	v_bitop3_b32 v43, v39, s3, 31 bitop3:0x6c
	v_cvt_f32_ubyte0_e32 v46, v43
	v_mul_u32_u24_e32 v43, 0x48, v37
	v_lshlrev_b32_e32 v43, 1, v43
	s_movk_i32 s3, 0x5f
	v_add3_u32 v48, s14, v34, v43
	v_bitop3_b32 v43, v39, s3, 31 bitop3:0x6c
	v_lshl_or_b32 v40, v110, 3, v112
	v_cvt_f32_ubyte0_e32 v47, v37
	v_or_b32_e32 v34, 32, v37
	v_cvt_f32_ubyte0_e32 v49, v43
	v_or_b32_e32 v43, 64, v37
	v_or_b32_e32 v37, 0x60, v37
	s_lshl_b32 s2, s15, 5
	v_cvt_f32_ubyte0_e32 v54, v37
	v_mul_u32_u24_e32 v37, 0x48, v40
	v_readlane_b32 s26, v233, 14
	v_readlane_b32 s27, v233, 15
	s_mov_b64 s[20:21], s[24:25]
	s_lshl_b32 s10, s76, 1
	s_add_i32 s2, s14, s2
	v_and_b32_e32 v41, 24, v119
	v_lshlrev_b32_e32 v42, 2, v110
	v_cvt_f32_ubyte0_e32 v50, v34
	v_bitop3_b32 v45, v39, 63, 31 bitop3:0x6c
	v_bitop3_b32 v39, v39, 31, v39 bitop3:0xc
	v_mul_u32_u24_e32 v34, 0x1a00, v34
	v_lshlrev_b32_e32 v37, 1, v37
	v_cvt_f32_ubyte0_e32 v51, v45
	v_cvt_f32_ubyte0_e32 v52, v43
	v_cvt_f32_ubyte0_e32 v53, v39
	v_add3_u32 v55, s2, v41, v37
	v_add3_u32 v56, s14, v41, v37
	s_add_i32 s11, s7, s10
	s_mov_b32 s18, 0xbfb8aa3b
	s_mov_b32 s19, 0x42ce8ed0
	s_mov_b32 s20, 0xc2b17218
	s_mov_b32 s21, 0x7f800000
	s_mov_b32 s22, 0x3f2aaaab
	v_mov_b32_e32 v57, 0x3ecc95a3
	s_mov_b32 s23, 0x3f317218
	s_mov_b32 s24, 0x33800000
	s_mov_b32 s25, 0x3fb8aa3b
	s_mov_b32 s26, 0xc2ce8ed0
	s_mov_b32 s27, 0x42b17218
	v_lshlrev_b32_e32 v36, 1, v36
	v_lshlrev_b32_e32 v38, 1, v38
	v_lshlrev_b32_e32 v40, 1, v34
	v_lshlrev_b32_e32 v34, 1, v44
	v_lshlrev_b32_e32 v42, 1, v42
	v_mov_b32_e32 v58, 0x7f800000
	v_mov_b32_e32 v44, 0x3f317218
	s_mov_b32 s34, s60
	v_mbcnt_lo_u32_b32 v231, -1, 0
	v_mbcnt_hi_u32_b32 v231, -1, v231
	v_and_b32_e32 v231, 15, v231
	v_lshlrev_b32_e32 v37, 2, v231
	global_load_dword v39, v37, s[12:13]
	s_waitcnt vmcnt(0)
	v_cmp_ngt_f32_e32 vcc, 0, v39
	s_and_saveexec_b64 s[98:99], vcc
	s_cbranch_execz .Llsv_rk1_a
	v_mul_f32_e32 v37, 0xbfb8aa3b, v39
	v_rndne_f32_e32 v41, v37
	v_sub_f32_e32 v43, v37, v41
	v_fma_f32 v37, v39, s18, -v37
	v_fmac_f32_e32 v37, 0xb2a5705f, v39
	v_add_f32_e32 v37, v43, v37
	v_cvt_i32_f32_e32 v41, v41
	v_exp_f32_e32 v37, v37
	v_cmp_nlt_f32_e32 vcc, s19, v39
	v_ldexp_f32 v37, v37, v41
	s_nop 0
	v_cndmask_b32_e32 v37, 0, v37, vcc
	v_cmp_ngt_f32_e32 vcc, s20, v39
	s_nop 1
	v_cndmask_b32_e32 v37, v58, v37, vcc
	v_add_f32_e32 v41, 1.0, v37
	v_add_f32_e32 v43, -1.0, v41
	v_sub_f32_e32 v45, v43, v41
	v_add_f32_e32 v45, 1.0, v45
	v_sub_f32_e32 v43, v37, v43
	v_add_f32_e32 v43, v43, v45
	v_frexp_mant_f32_e32 v45, v41
	v_cvt_f64_f32_e32 v[60:61], v41
	v_frexp_exp_i32_f64_e32 v59, v[60:61]
	v_cmp_gt_f32_e32 vcc, s22, v45
	s_nop 1
	v_subbrev_co_u32_e32 v59, vcc, 0, v59, vcc
	v_sub_u32_e32 v45, 0, v59
	v_ldexp_f32 v41, v41, v45
	v_ldexp_f32 v43, v43, v45
	v_add_f32_e32 v45, -1.0, v41
	v_add_f32_e32 v61, 1.0, v41
	v_add_f32_e32 v60, 1.0, v45
	v_add_f32_e32 v62, -1.0, v61
	v_sub_f32_e32 v60, v41, v60
	v_sub_f32_e32 v41, v41, v62
	v_add_f32_e32 v41, v43, v41
	v_add_f32_e32 v60, v43, v60
	v_add_f32_e32 v43, v61, v41
	v_rcp_f32_e32 v68, v43
	v_sub_f32_e32 v61, v61, v43
	v_add_f32_e32 v41, v41, v61
	v_add_f32_e32 v61, v45, v60
	v_mul_f32_e32 v69, v61, v68
	v_mul_f32_e32 v62, v43, v69
	v_fma_f32 v64, v69, v43, -v62
	v_sub_f32_e32 v45, v45, v61
	v_fmac_f32_e32 v64, v69, v41
	v_add_f32_e32 v45, v60, v45
	v_add_f32_e32 v60, v62, v64
	v_sub_f32_e32 v63, v61, v60
	v_pk_add_f32 v[66:67], v[60:61], v[62:63] neg_lo:[0,1] neg_hi:[0,1]
	v_mov_b32_e32 v65, v60
	v_pk_add_f32 v[60:61], v[66:67], v[64:65] neg_lo:[0,1] neg_hi:[0,1]
	v_cmp_neq_f32_e32 vcc, s21, v37
	v_add_f32_e32 v45, v45, v61
	v_add_f32_e32 v45, v60, v45
	v_add_f32_e32 v61, v63, v45
	v_mul_f32_e32 v70, v68, v61
	v_mul_f32_e32 v62, v43, v70
	v_fma_f32 v64, v70, v43, -v62
	v_fmac_f32_e32 v64, v70, v41
	v_add_f32_e32 v60, v62, v64
	v_sub_f32_e32 v41, v63, v61
	v_sub_f32_e32 v63, v61, v60
	v_pk_add_f32 v[66:67], v[60:61], v[62:63] neg_lo:[0,1] neg_hi:[0,1]
	v_mov_b32_e32 v65, v60
	v_add_f32_e32 v41, v45, v41
	v_pk_add_f32 v[60:61], v[66:67], v[64:65] neg_lo:[0,1] neg_hi:[0,1]
	v_add_f32_e32 v43, v69, v70
	v_add_f32_e32 v41, v41, v61
	v_add_f32_e32 v41, v60, v41
	v_add_f32_e32 v41, v63, v41
	v_sub_f32_e32 v45, v43, v69
	v_mul_f32_e32 v41, v68, v41
	v_sub_f32_e32 v45, v70, v45
	v_add_f32_e32 v41, v45, v41
	v_add_f32_e32 v61, v43, v41
	v_cvt_f32_i32_e32 v60, v59
	v_mul_f32_e32 v62, v61, v61
	v_fmamk_f32 v45, v62, 0x3e9b6dac, v57
	v_fmaak_f32 v45, v62, v45, 0x3f2aaada
	v_sub_f32_e32 v43, v61, v43
	v_ldexp_f32 v63, v61, 1
	v_mul_f32_e32 v61, v61, v62
	v_pk_mul_f32 v[64:65], v[60:61], v[44:45]
	v_sub_f32_e32 v41, v41, v43
	v_fma_f32 v62, v60, s23, -v64
	v_fmac_f32_e32 v62, 0xb102e308, v60
	v_pk_add_f32 v[60:61], v[64:65], v[62:63]
	v_ldexp_f32 v41, v41, 1
	v_sub_f32_e32 v43, v61, v63
	v_sub_f32_e32 v43, v65, v43
	v_add_f32_e32 v67, v41, v43
	v_mov_b32_e32 v66, v64
	v_pk_add_f32 v[64:65], v[60:61], v[64:65] neg_lo:[0,1] neg_hi:[0,1]
	v_pk_add_f32 v[68:69], v[60:61], v[66:67]
	v_mov_b32_e32 v63, v60
	v_mov_b32_e32 v65, v69
	v_pk_add_f32 v[70:71], v[62:63], v[64:65] neg_lo:[0,1] neg_hi:[0,1]
	v_pk_add_f32 v[62:63], v[62:63], v[64:65]
	v_mov_b32_e32 v74, v61
	v_pk_add_f32 v[64:65], v[62:63], v[60:61] op_sel:[1,0] op_sel_hi:[0,1] neg_lo:[0,1] neg_hi:[0,1]
	v_pk_add_f32 v[72:73], v[68:69], v[64:65] op_sel_hi:[1,0] neg_lo:[0,1] neg_hi:[0,1]
	v_mov_b32_e32 v68, v69
	v_mov_b32_e32 v69, v63
	v_mov_b32_e32 v75, v64
	v_pk_add_f32 v[64:65], v[68:69], v[74:75] neg_lo:[0,1] neg_hi:[0,1]
	v_mov_b32_e32 v66, v67
	v_mov_b32_e32 v67, v60
	v_pk_add_f32 v[60:61], v[66:67], v[64:65] neg_lo:[0,1] neg_hi:[0,1]
	v_mov_b32_e32 v72, v70
	v_pk_add_f32 v[64:65], v[72:73], v[60:61]
	v_mov_b32_e32 v71, v63
	v_pk_add_f32 v[66:67], v[64:65], v[64:65] op_sel:[0,1] op_sel_hi:[1,0]
	s_nop 0
	v_pk_add_f32 v[62:63], v[62:63], v[66:67] op_sel:[1,0] op_sel_hi:[0,1]
	v_mov_b32_e32 v65, v62
	v_pk_add_f32 v[68:69], v[64:65], v[70:71] neg_lo:[0,1] neg_hi:[0,1]
	v_mov_b32_e32 v61, v66
	v_sub_f32_e32 v41, v64, v68
	v_pk_add_f32 v[60:61], v[60:61], v[68:69] neg_lo:[0,1] neg_hi:[0,1]
	v_sub_f32_e32 v41, v70, v41
	v_add_f32_e32 v41, v60, v41
	v_add_f32_e32 v41, v41, v61
	v_add_f32_e32 v41, v62, v41
	v_cndmask_b32_e32 v41, v58, v41, vcc
	v_cmp_lt_f32_e64 vcc, |v37|, s24
	s_nop 1
	v_cndmask_b32_e32 v37, v41, v37, vcc
	v_xor_b32_e32 v37, 0x80000000, v37
.Llsv_rk1_a:
	s_xor_b64 exec, exec, s[98:99]
	s_cbranch_execz .Llsv_rk1_b
	v_mul_f32_e32 v37, 0x3fb8aa3b, v39
	v_rndne_f32_e32 v41, v37
	v_sub_f32_e32 v43, v37, v41
	v_fma_f32 v37, v39, s25, -v37
	v_fmac_f32_e32 v37, 0x32a5705f, v39
	v_add_f32_e32 v37, v43, v37
	v_cvt_i32_f32_e32 v41, v41
	v_exp_f32_e32 v37, v37
	v_cmp_ngt_f32_e32 vcc, s26, v39
	v_ldexp_f32 v37, v37, v41
	s_nop 0
	v_cndmask_b32_e32 v37, 0, v37, vcc
	v_cmp_nlt_f32_e32 vcc, s27, v39
	s_nop 1
	v_cndmask_b32_e32 v37, v58, v37, vcc
	v_add_f32_e32 v41, 1.0, v37
	v_add_f32_e32 v43, -1.0, v41
	v_sub_f32_e32 v45, v43, v41
	v_add_f32_e32 v45, 1.0, v45
	v_sub_f32_e32 v43, v37, v43
	v_add_f32_e32 v43, v43, v45
	v_frexp_mant_f32_e32 v45, v41
	v_cvt_f64_f32_e32 v[60:61], v41
	v_frexp_exp_i32_f64_e32 v59, v[60:61]
	v_cmp_gt_f32_e32 vcc, s22, v45
	s_nop 1
	v_subbrev_co_u32_e32 v59, vcc, 0, v59, vcc
	v_sub_u32_e32 v45, 0, v59
	v_ldexp_f32 v41, v41, v45
	v_ldexp_f32 v43, v43, v45
	v_add_f32_e32 v45, -1.0, v41
	v_add_f32_e32 v61, 1.0, v41
	v_add_f32_e32 v60, 1.0, v45
	v_add_f32_e32 v62, -1.0, v61
	v_sub_f32_e32 v60, v41, v60
	v_sub_f32_e32 v41, v41, v62
	v_add_f32_e32 v41, v43, v41
	v_add_f32_e32 v60, v43, v60
	v_add_f32_e32 v43, v61, v41
	v_rcp_f32_e32 v68, v43
	v_sub_f32_e32 v61, v61, v43
	v_add_f32_e32 v41, v41, v61
	v_add_f32_e32 v61, v45, v60
	v_mul_f32_e32 v69, v61, v68
	v_mul_f32_e32 v62, v43, v69
	v_fma_f32 v64, v69, v43, -v62
	v_sub_f32_e32 v45, v45, v61
	v_fmac_f32_e32 v64, v69, v41
	v_add_f32_e32 v45, v60, v45
	v_add_f32_e32 v60, v62, v64
	v_sub_f32_e32 v63, v61, v60
	v_pk_add_f32 v[66:67], v[60:61], v[62:63] neg_lo:[0,1] neg_hi:[0,1]
	v_mov_b32_e32 v65, v60
	v_pk_add_f32 v[60:61], v[66:67], v[64:65] neg_lo:[0,1] neg_hi:[0,1]
	v_cmp_neq_f32_e32 vcc, s21, v37
	v_add_f32_e32 v45, v45, v61
	v_add_f32_e32 v45, v60, v45
	v_add_f32_e32 v61, v63, v45
	v_mul_f32_e32 v70, v68, v61
	v_mul_f32_e32 v62, v43, v70
	v_fma_f32 v64, v70, v43, -v62
	v_fmac_f32_e32 v64, v70, v41
	v_add_f32_e32 v60, v62, v64
	v_sub_f32_e32 v41, v63, v61
	v_sub_f32_e32 v63, v61, v60
	v_pk_add_f32 v[66:67], v[60:61], v[62:63] neg_lo:[0,1] neg_hi:[0,1]
	v_mov_b32_e32 v65, v60
	v_add_f32_e32 v41, v45, v41
	v_pk_add_f32 v[60:61], v[66:67], v[64:65] neg_lo:[0,1] neg_hi:[0,1]
	v_add_f32_e32 v43, v69, v70
	v_add_f32_e32 v41, v41, v61
	v_add_f32_e32 v41, v60, v41
	v_add_f32_e32 v41, v63, v41
	v_sub_f32_e32 v45, v43, v69
	v_mul_f32_e32 v41, v68, v41
	v_sub_f32_e32 v45, v70, v45
	v_add_f32_e32 v41, v45, v41
	v_add_f32_e32 v61, v43, v41
	v_cvt_f32_i32_e32 v60, v59
	v_mul_f32_e32 v62, v61, v61
	v_fmamk_f32 v45, v62, 0x3e9b6dac, v57
	v_fmaak_f32 v45, v62, v45, 0x3f2aaada
	v_sub_f32_e32 v43, v61, v43
	v_ldexp_f32 v63, v61, 1
	v_mul_f32_e32 v61, v61, v62
	v_pk_mul_f32 v[64:65], v[60:61], v[44:45]
	v_sub_f32_e32 v41, v41, v43
	v_fma_f32 v62, v60, s23, -v64
	v_fmac_f32_e32 v62, 0xb102e308, v60
	v_pk_add_f32 v[60:61], v[64:65], v[62:63]
	v_ldexp_f32 v41, v41, 1
	v_sub_f32_e32 v43, v61, v63
	v_sub_f32_e32 v43, v65, v43
	v_add_f32_e32 v67, v41, v43
	v_mov_b32_e32 v66, v64
	v_pk_add_f32 v[64:65], v[60:61], v[64:65] neg_lo:[0,1] neg_hi:[0,1]
	v_pk_add_f32 v[68:69], v[60:61], v[66:67]
	v_mov_b32_e32 v63, v60
	v_mov_b32_e32 v65, v69
	v_pk_add_f32 v[70:71], v[62:63], v[64:65] neg_lo:[0,1] neg_hi:[0,1]
	v_pk_add_f32 v[62:63], v[62:63], v[64:65]
	v_mov_b32_e32 v74, v61
	v_pk_add_f32 v[64:65], v[62:63], v[60:61] op_sel:[1,0] op_sel_hi:[0,1] neg_lo:[0,1] neg_hi:[0,1]
	v_pk_add_f32 v[72:73], v[68:69], v[64:65] op_sel_hi:[1,0] neg_lo:[0,1] neg_hi:[0,1]
	v_mov_b32_e32 v68, v69
	v_mov_b32_e32 v69, v63
	v_mov_b32_e32 v75, v64
	v_pk_add_f32 v[64:65], v[68:69], v[74:75] neg_lo:[0,1] neg_hi:[0,1]
	v_mov_b32_e32 v66, v67
	v_mov_b32_e32 v67, v60
	v_pk_add_f32 v[60:61], v[66:67], v[64:65] neg_lo:[0,1] neg_hi:[0,1]
	v_mov_b32_e32 v72, v70
	v_pk_add_f32 v[64:65], v[72:73], v[60:61]
	v_mov_b32_e32 v71, v63
	v_pk_add_f32 v[66:67], v[64:65], v[64:65] op_sel:[0,1] op_sel_hi:[1,0]
	s_nop 0
	v_pk_add_f32 v[62:63], v[62:63], v[66:67] op_sel:[1,0] op_sel_hi:[0,1]
	v_mov_b32_e32 v65, v62
	v_pk_add_f32 v[68:69], v[64:65], v[70:71] neg_lo:[0,1] neg_hi:[0,1]
	v_mov_b32_e32 v61, v66
	v_sub_f32_e32 v41, v64, v68
	v_pk_add_f32 v[60:61], v[60:61], v[68:69] neg_lo:[0,1] neg_hi:[0,1]
	v_sub_f32_e32 v41, v70, v41
	v_add_f32_e32 v41, v60, v41
	v_add_f32_e32 v41, v41, v61
	v_add_f32_e32 v41, v62, v41
	v_cndmask_b32_e32 v41, v58, v41, vcc
	v_cmp_gt_f32_e32 vcc, s24, v37
	s_nop 1
	v_cndmask_b32_e32 v37, v41, v37, vcc
	v_sub_f32_e32 v37, v39, v37

.LBB0_3590:
	s_or_b64 exec, exec, s[4:5]
	s_mov_b32 s0, 1
	s_mov_b64 s[4:5], s[74:75]
	v_mov_b32_e32 v70, v0
	s_waitcnt lgkmcnt(0)
	s_barrier
	s_nop 0
	v_writelane_b32 v232, s0, 49
	v_readfirstlane_b32 s8, v70
	s_nop 0
	v_writelane_b32 v232, s1, 50
	s_mov_b64 s[0:1], -1
	v_readlane_b32 s2, v232, 44
	v_readlane_b32 s3, v232, 45
	s_and_b64 vcc, exec, s[2:3]
	s_cbranch_vccz .LBB0_3614
	v_writelane_b32 v232, s8, 25
	v_writelane_b32 v232, s60, 24
	v_writelane_b32 v232, s93, 23
	s_add_u32 s80, s4, 0x16400000
	v_writelane_b32 v232, s94, 54
	s_addc_u32 s81, s5, 0
	s_add_i32 s2, s96, 0xffffff80
	v_writelane_b32 v232, s95, 55
	s_add_i32 s90, s76, 0xffffff80
	s_mov_b32 s0, s2
	v_writelane_b32 v232, s0, 21
	s_cmpk_gt_u32 s2, 0x3ff
	v_readfirstlane_b32 s6, v70
	v_writelane_b32 v232, s1, 22
	s_cbranch_scc1 .LBB0_3604
	v_readlane_b32 s0, v232, 49
	v_readlane_b32 s1, v232, 50
	s_mov_b32 s2, s0
	s_lshl_b32 s0, s0, 4
	s_ashr_i32 s1, s0, 31
	v_readlane_b32 s8, v233, 0
	s_lshl_b64 s[0:1], s[0:1], 2
	v_readlane_b32 s18, v233, 10
	v_readlane_b32 s19, v233, 11
	s_add_u32 s82, s18, s0
	s_addc_u32 s83, s19, s1
	s_lshl_b32 s0, s2, 9
	s_ashr_i32 s1, s0, 31
	v_readlane_b32 s20, v233, 12
	s_lshl_b64 s[0:1], s[0:1], 2
	v_readlane_b32 s21, v233, 13
	s_add_u32 s0, s20, s0
	s_addc_u32 s1, s21, s1
	s_add_u32 s84, s4, 0x1a400000
	s_addc_u32 s85, s5, 0
	v_readlane_b32 s9, v233, 1
	s_add_u32 s77, s4, 0x29400000
	v_readlane_b32 s2, v232, 51
	v_readlane_b32 s88, v232, 21
	s_addc_u32 s91, s5, 0
	v_readlane_b32 s3, v232, 52
	s_and_b32 s7, s2, 31
	s_lshr_b32 s9, s88, 8
	s_lshl_b32 s2, s9, 12
	s_lshl_b32 s3, s7, 7
	s_or_b32 s2, s2, s3
	s_bfe_u32 s8, s88, 0x30005
	s_mulk_i32 s2, 0x3400
	v_readlane_b32 s10, v233, 2
	s_add_u32 s2, s84, s2
	s_addc_u32 s3, s85, 0
	s_lshl_b32 s10, s8, 7
	s_add_u32 s2, s2, s10
	s_addc_u32 s3, s3, 0
	s_lshl_b32 s9, s9, 4
	s_lshl_b32 s8, s8, 1
	s_or_b32 s10, s8, s9
	s_lshl_b32 s8, s10, 18
	s_lshl_b32 s9, s7, 13
	s_or_b32 s8, s8, s9
	s_add_u32 s8, s77, s8
	s_addc_u32 s9, s91, 0
	s_lshl_b32 s10, s10, 5
	s_or_b32 s7, s10, s7
	v_readlane_b32 s11, v233, 3
	s_mov_b32 s87, 0
	s_or_b32 s86, s7, 32
	s_lshl_b64 s[10:11], s[86:87], 13
	s_waitcnt vmcnt(0)
	v_lshlrev_b32_e32 v1, 3, v70
	v_lshlrev_b32_e32 v29, 2, v70
	v_add_u32_e32 v38, 0x200, v70
	s_add_u32 s10, s77, s10
	v_and_b32_e32 v26, 56, v1
	v_mov_b32_e32 v73, 0
	v_and_b32_e32 v28, 60, v29
	v_and_b32_e32 v16, 0xffffffc0, v29
	v_lshlrev_b32_e32 v36, 2, v38
	s_addc_u32 s11, s91, s11
	v_lshlrev_b32_e32 v72, 1, v26
	v_lshlrev_b32_e32 v30, 1, v28
	v_mov_b32_e32 v31, v73
	v_ashrrev_i32_e32 v17, 31, v16
	v_and_b32_e32 v36, 0xffffffc0, v36
	s_movk_i32 s95, 0x3400
	v_lshl_add_u64 v[14:15], s[2:3], 0, v[72:73]
	v_lshl_add_u64 v[32:33], s[8:9], 0, v[30:31]
	v_lshl_add_u64 v[34:35], s[10:11], 0, v[30:31]
	v_ashrrev_i32_e32 v31, 3, v70
	v_lshlrev_b64 v[76:77], 1, v[16:17]
	v_ashrrev_i32_e32 v37, 31, v36
	v_mad_i64_i32 v[10:11], s[2:3], v31, s95, v[14:15]
	v_lshl_add_u64 v[16:17], v[32:33], 0, v[76:77]
	v_ashrrev_i32_e32 v39, 3, v38
	v_lshlrev_b64 v[80:81], 1, v[36:37]
	global_load_dwordx4 v[2:5], v[10:11], off
	global_load_dwordx4 v[6:9], v[10:11], off offset:1024
	s_nop 0
	global_load_dwordx4 v[10:13], v[10:11], off offset:2048
	v_mad_i64_i32 v[22:23], s[2:3], v39, s95, v[14:15]
	global_load_dwordx2 v[94:95], v[16:17], off
	v_lshl_add_u64 v[16:17], v[34:35], 0, v[76:77]
	v_lshl_add_u64 v[32:33], v[32:33], 0, v[80:81]
	global_load_dwordx2 v[96:97], v[16:17], off
	s_nop 0
	global_load_dwordx4 v[14:17], v[22:23], off
	global_load_dwordx4 v[18:21], v[22:23], off offset:1024
	s_nop 0
	global_load_dwordx4 v[22:25], v[22:23], off offset:2048
	v_mad_i64_i32 v[74:75], s[2:3], v31, s95, 0
	global_load_dwordx2 v[98:99], v[32:33], off
	v_lshl_add_u64 v[32:33], v[34:35], 0, v[80:81]
	global_load_dwordx2 v[100:101], v[32:33], off
	v_mad_i64_i32 v[78:79], s[2:3], v39, s95, 0
	s_ashr_i32 s2, s6, 2
	s_nop 0
	v_bfi_b32 v82, -16, s2, v70
	s_movk_i32 s2, 0x90
	v_add_u32_e32 v34, 0, v30
	v_mul_lo_u32 v30, v82, s2
	v_add_u32_e32 v33, 0, v30
	v_lshrrev_b32_e32 v30, 2, v70
	v_and_b32_e32 v30, 12, v30
	v_sub_u32_e32 v41, 0x80, v82
	v_add_u32_e32 v32, 0, v72
	s_movk_i32 s3, 0x80
	v_cvt_f32_i32_e32 v71, v41
	v_bfrev_b32_e32 v41, 0.5
	v_lshlrev_b32_e32 v72, 2, v30
	v_and_b32_e32 v35, 48, v70
	v_bitop3_b32 v116, v29, 64, v41 bitop3:0x6c
	v_bitop3_b32 v117, v29, s3, v41 bitop3:0x6c
	v_lshl_add_u64 v[84:85], s[0:1], 0, v[72:73]
	v_mad_u64_u32 v[86:87], s[0:1], v31, s2, v[32:33]
	v_lshrrev_b32_e32 v29, 4, v70
	v_sub_u32_e32 v31, v82, v30
	v_mad_u64_u32 v[88:89], s[0:1], v29, s2, v[34:35]
	v_cvt_f32_i32_e32 v87, v31
	v_sub_u32_e32 v31, v30, v82
	v_lshrrev_b32_e32 v29, 4, v38
	v_cvt_f32_i32_e32 v89, v31
	v_or_b32_e32 v31, 1, v30
	v_mad_u64_u32 v[90:91], s[0:1], v39, s2, v[32:33]
	v_mad_u64_u32 v[92:93], s[0:1], v29, s2, v[34:35]
	v_sub_u32_e32 v32, v31, v82
	v_sub_u32_e32 v31, v82, v31
	v_readlane_b32 s14, v233, 6
	v_readlane_b32 s15, v233, 7
	v_cvt_f32_i32_e32 v93, v31
	v_or_b32_e32 v31, 2, v30
	v_cvt_f32_i32_e32 v91, v32
	v_cmp_gt_i32_e64 s[14:15], v31, v82
	v_sub_u32_e32 v32, v82, v31
	v_sub_u32_e32 v31, v31, v82
	v_readlane_b32 s16, v233, 8
	v_readlane_b32 s17, v233, 9
	v_cvt_f32_i32_e32 v119, v31
	v_or_b32_e32 v31, 3, v30
	v_cvt_f32_i32_e32 v118, v32
	v_cmp_gt_i32_e64 s[16:17], v31, v82
	v_sub_u32_e32 v32, v82, v31
	v_sub_u32_e32 v31, v31, v82
	v_cvt_f32_i32_e32 v121, v31
	v_or_b32_e32 v31, 16, v30
	v_cvt_f32_i32_e32 v120, v32
	v_cmp_gt_i32_e64 s[18:19], v31, v82
	v_sub_u32_e32 v32, v82, v31
	v_sub_u32_e32 v31, v31, v82
	v_cvt_f32_i32_e32 v123, v31
	v_or_b32_e32 v31, 17, v30
	v_cvt_f32_i32_e32 v122, v32
	v_cmp_gt_i32_e64 s[20:21], v31, v82
	v_sub_u32_e32 v32, v82, v31
	v_sub_u32_e32 v31, v31, v82
	v_readlane_b32 s22, v233, 14
	v_readlane_b32 s23, v233, 15
	v_cvt_f32_i32_e32 v125, v31
	v_or_b32_e32 v31, 18, v30
	v_cvt_f32_i32_e32 v124, v32
	v_cmp_gt_i32_e64 s[22:23], v31, v82
	v_sub_u32_e32 v32, v82, v31
	v_sub_u32_e32 v31, v31, v82
	v_cvt_f32_i32_e32 v127, v31
	v_or_b32_e32 v31, 19, v30
	v_cvt_f32_i32_e32 v126, v32
	v_cmp_gt_i32_e64 s[24:25], v31, v82
	v_sub_u32_e32 v32, v82, v31
	v_sub_u32_e32 v31, v31, v82
	v_cvt_f32_i32_e32 v129, v31
	v_or_b32_e32 v31, 32, v30
	v_cvt_f32_i32_e32 v128, v32
	v_sub_u32_e32 v32, v82, v31
	v_cvt_f32_i32_e32 v130, v32
	v_sub_u32_e32 v32, v31, v82
	v_cvt_f32_i32_e32 v131, v32
	v_or_b32_e32 v32, 33, v30
	v_cmp_gt_i32_e64 s[28:29], v32, v82
	v_sub_u32_e32 v34, v82, v32
	v_sub_u32_e32 v32, v32, v82
	v_cvt_f32_i32_e32 v133, v32
	v_or_b32_e32 v32, 34, v30
	v_cvt_f32_i32_e32 v132, v34
	v_cmp_gt_i32_e64 s[30:31], v32, v82
	v_sub_u32_e32 v34, v82, v32
	v_sub_u32_e32 v32, v32, v82
	v_cvt_f32_i32_e32 v135, v32
	v_or_b32_e32 v32, 35, v30
	v_cvt_f32_i32_e32 v134, v34
	v_cmp_gt_i32_e64 s[34:35], v32, v82
	v_sub_u32_e32 v34, v82, v32
	v_sub_u32_e32 v32, v32, v82
	v_cvt_f32_i32_e32 v137, v32
	v_or_b32_e32 v32, 48, v30
	v_cvt_f32_i32_e32 v136, v34
	v_cmp_gt_i32_e64 s[36:37], v32, v82
	v_sub_u32_e32 v34, v82, v32
	v_sub_u32_e32 v32, v32, v82
	v_cvt_f32_i32_e32 v139, v32
	v_or_b32_e32 v32, 49, v30
	v_cvt_f32_i32_e32 v138, v34
	v_cmp_gt_i32_e64 s[38:39], v32, v82
	v_sub_u32_e32 v34, v82, v32
	v_sub_u32_e32 v32, v32, v82
	v_cvt_f32_i32_e32 v141, v32
	v_or_b32_e32 v32, 50, v30
	v_cvt_f32_i32_e32 v140, v34
	v_cmp_gt_i32_e64 s[40:41], v32, v82
	v_sub_u32_e32 v34, v82, v32
	v_sub_u32_e32 v32, v32, v82
	v_cvt_f32_i32_e32 v143, v32
	v_or_b32_e32 v32, 51, v30
	v_cvt_f32_i32_e32 v142, v34
	v_cmp_gt_i32_e64 s[42:43], v32, v82
	v_sub_u32_e32 v34, v82, v32
	v_sub_u32_e32 v32, v32, v82
	v_cvt_f32_i32_e32 v145, v32
	v_or_b32_e32 v32, 64, v30
	v_cvt_f32_i32_e32 v144, v34
	v_sub_u32_e32 v34, v82, v32
	v_cvt_f32_i32_e32 v146, v34
	v_sub_u32_e32 v34, v32, v82
	v_cvt_f32_i32_e32 v147, v34
	v_or_b32_e32 v34, 0x41, v30
	v_cmp_gt_i32_e64 s[46:47], v34, v82
	v_sub_u32_e32 v38, v82, v34
	v_sub_u32_e32 v34, v34, v82
	v_cvt_f32_i32_e32 v149, v34
	v_or_b32_e32 v34, 0x42, v30
	v_cvt_f32_i32_e32 v148, v38
	v_cmp_gt_i32_e64 s[48:49], v34, v82
	v_sub_u32_e32 v38, v82, v34
	v_sub_u32_e32 v34, v34, v82
	v_cvt_f32_i32_e32 v151, v34
	v_or_b32_e32 v34, 0x43, v30
	v_cvt_f32_i32_e32 v150, v38
	v_cmp_gt_i32_e64 s[50:51], v34, v82
	v_sub_u32_e32 v38, v82, v34
	v_sub_u32_e32 v34, v34, v82
	v_cvt_f32_i32_e32 v153, v34
	v_or_b32_e32 v34, 0x50, v30
	v_cvt_f32_i32_e32 v152, v38
	v_cmp_gt_i32_e64 s[52:53], v34, v82
	v_sub_u32_e32 v38, v82, v34
	v_sub_u32_e32 v34, v34, v82
	v_cvt_f32_i32_e32 v155, v34
	v_or_b32_e32 v34, 0x51, v30
	v_cvt_f32_i32_e32 v154, v38
	v_cmp_gt_i32_e64 s[54:55], v34, v82
	v_sub_u32_e32 v38, v82, v34
	v_sub_u32_e32 v34, v34, v82
	v_cvt_f32_i32_e32 v157, v34
	v_or_b32_e32 v34, 0x52, v30
	v_cvt_f32_i32_e32 v156, v38
	v_cmp_gt_i32_e64 s[56:57], v34, v82
	v_sub_u32_e32 v38, v82, v34
	v_sub_u32_e32 v34, v34, v82
	v_cvt_f32_i32_e32 v159, v34
	v_or_b32_e32 v34, 0x53, v30
	v_cvt_f32_i32_e32 v158, v38
	v_cmp_gt_i32_e64 s[58:59], v34, v82
	v_sub_u32_e32 v38, v82, v34
	v_sub_u32_e32 v34, v34, v82
	v_cvt_f32_i32_e32 v161, v34
	v_or_b32_e32 v34, 0x60, v30
	v_cvt_f32_i32_e32 v160, v38
	v_sub_u32_e32 v38, v82, v34
	v_cvt_f32_i32_e32 v162, v38
	v_sub_u32_e32 v38, v34, v82
	v_cvt_f32_i32_e32 v163, v38
	v_or_b32_e32 v38, 0x61, v30
	v_cmp_gt_i32_e64 s[62:63], v38, v82
	v_sub_u32_e32 v39, v82, v38
	v_sub_u32_e32 v38, v38, v82
	v_cvt_f32_i32_e32 v165, v38
	v_or_b32_e32 v38, 0x62, v30
	v_cvt_f32_i32_e32 v164, v39
	v_cmp_gt_i32_e64 s[64:65], v38, v82
	v_sub_u32_e32 v39, v82, v38
	v_sub_u32_e32 v38, v38, v82
	v_cvt_f32_i32_e32 v167, v38
	v_or_b32_e32 v38, 0x63, v30
	v_cvt_f32_i32_e32 v166, v39
	v_cmp_gt_i32_e64 s[66:67], v38, v82
	v_sub_u32_e32 v39, v82, v38
	v_sub_u32_e32 v38, v38, v82
	v_cvt_f32_i32_e32 v169, v38
	v_or_b32_e32 v38, 0x70, v30
	v_cvt_f32_i32_e32 v168, v39
	v_cmp_gt_i32_e64 s[68:69], v38, v82
	v_sub_u32_e32 v39, v82, v38
	v_sub_u32_e32 v38, v38, v82
	v_cvt_f32_i32_e32 v171, v38
	v_or_b32_e32 v38, 0x71, v30
	v_cvt_f32_i32_e32 v170, v39
	v_cmp_gt_i32_e64 s[70:71], v38, v82
	v_sub_u32_e32 v39, v82, v38
	v_sub_u32_e32 v38, v38, v82
	v_cvt_f32_i32_e32 v173, v38
	v_or_b32_e32 v38, 0x72, v30
	v_cvt_f32_i32_e32 v172, v39
	v_cmp_gt_i32_e64 s[72:73], v38, v82
	v_sub_u32_e32 v39, v82, v38
	v_sub_u32_e32 v38, v38, v82
	v_and_b32_e32 v1, 24, v1
	v_cvt_f32_i32_e32 v175, v38
	v_or_b32_e32 v38, 0x73, v30
	v_add_u32_e32 v40, 0, v1
	v_add_u32_e32 v1, 1, v82
	v_cvt_f32_i32_e32 v174, v39
	v_cmp_gt_i32_e64 s[74:75], v38, v82
	v_sub_u32_e32 v39, v82, v38
	v_sub_u32_e32 v38, v38, v82
	v_and_b32_e32 v27, 15, v70
	v_bfe_u32 v37, v70, 2, 2
	v_cvt_f32_i32_e32 v1, v1
	v_cvt_f32_i32_e32 v176, v39
	v_cvt_f32_i32_e32 v177, v38
	v_add_u32_e32 v36, 0, v35
	v_mul_u32_u24_e32 v29, 0x90, v27
	v_cmp_gt_i32_e64 s[26:27], v31, v82
	v_cmp_gt_i32_e64 s[44:45], v32, v82
	v_cmp_gt_i32_e64 s[60:61], v34, v82
	v_or_b32_e32 v38, v30, v37
	v_or_b32_e32 v31, v31, v37
	v_or_b32_e32 v32, v32, v37
	v_or_b32_e32 v34, v34, v37
	v_mul_u32_u24_e32 v27, 0x48, v27
	v_readlane_b32 s12, v233, 4
	v_readlane_b32 s13, v233, 5
	v_mul_u32_u24_e32 v38, 0x90, v38
	v_mul_u32_u24_e32 v31, 0x90, v31
	v_mul_u32_u24_e32 v32, 0x90, v32
	v_mul_u32_u24_e32 v34, 0x90, v34
	v_lshl_add_u32 v178, v27, 1, v36
	v_ashrrev_i32_e32 v83, 31, v82
	v_cmp_gt_i32_e64 s[6:7], v30, v82
	v_cmp_lt_i32_e64 s[12:13], v30, v82
	v_add_u32_e32 v179, 0x900, v178
	v_add_u32_e32 v180, 0x1200, v178
	v_add_u32_e32 v181, 0x1b00, v178
	s_mov_b32 s8, 0xbfb8aa3b
	s_mov_b32 s9, 0x42ce8ed0
	s_mov_b32 s10, 0xc2b17218
	s_mov_b32 s94, 0x7f800000
	s_mov_b32 s78, 0x3f2aaaab
	v_mov_b32_e32 v182, 0x3ecc95a3
	s_mov_b32 s11, 0x3f317218
	s_mov_b32 s76, 0x33800000
	s_mov_b32 s79, 0x3fb8aa3b
	v_lshlrev_b32_e32 v102, 1, v26
	v_lshlrev_b32_e32 v104, 1, v28
	v_add_u32_e32 v183, v33, v35
	v_add_u32_e32 v184, v36, v29
	v_add_u32_e32 v185, v40, v38
	v_add_u32_e32 v186, v40, v31
	v_add_u32_e32 v187, v40, v32
	v_add_u32_e32 v188, v40, v34
	v_lshlrev_b32_e32 v72, 1, v30
	v_mov_b32_e32 v189, 0x3a27c5ac
	v_mov_b32_e32 v190, 0x260
	v_mov_b32_e32 v191, 0x7f800000
	v_mov_b32_e32 v106, 0x3f317218
	s_mov_b32 s86, s88
	v_readlane_b32 s89, v232, 22
	v_mbcnt_lo_u32_b32 v221, -1, 0
	v_mbcnt_hi_u32_b32 v221, -1, v221
	v_and_b32_e32 v221, 15, v221
	v_lshlrev_b32_e32 v26, 2, v221
	global_load_dword v26, v26, s[82:83]
	s_waitcnt vmcnt(0)
	v_cmp_ngt_f32_e32 vcc, 0, v26
	s_and_saveexec_b64 s[98:99], vcc
	s_cbranch_execz .Llsv_ro1_a
	v_mul_f32_e32 v27, 0xbfb8aa3b, v26
	v_rndne_f32_e32 v28, v27
	v_sub_f32_e32 v29, v27, v28
	v_fma_f32 v27, v26, s8, -v27
	v_fmac_f32_e32 v27, 0xb2a5705f, v26
	v_add_f32_e32 v27, v29, v27
	v_cvt_i32_f32_e32 v28, v28
	v_exp_f32_e32 v27, v27
	v_cmp_nlt_f32_e32 vcc, s9, v26
	v_ldexp_f32 v27, v27, v28
	s_nop 0
	v_cndmask_b32_e32 v27, 0, v27, vcc
	v_cmp_ngt_f32_e32 vcc, s10, v26
	s_nop 1
	v_cndmask_b32_e32 v27, v191, v27, vcc
	v_add_f32_e32 v30, 1.0, v27
	v_add_f32_e32 v28, -1.0, v30
	v_sub_f32_e32 v29, v28, v30
	v_add_f32_e32 v29, 1.0, v29
	v_sub_f32_e32 v28, v27, v28
	v_add_f32_e32 v31, v28, v29
	v_frexp_mant_f32_e32 v32, v30
	v_cvt_f64_f32_e32 v[28:29], v30
	v_frexp_exp_i32_f64_e32 v28, v[28:29]
	v_cmp_gt_f32_e32 vcc, s78, v32
	s_nop 1
	v_subbrev_co_u32_e32 v36, vcc, 0, v28, vcc
	v_sub_u32_e32 v28, 0, v36
	v_ldexp_f32 v29, v30, v28
	v_add_f32_e32 v30, -1.0, v29
	v_add_f32_e32 v32, 1.0, v29
	v_ldexp_f32 v28, v31, v28
	v_add_f32_e32 v31, 1.0, v30
	v_add_f32_e32 v33, -1.0, v32
	v_sub_f32_e32 v31, v29, v31
	v_sub_f32_e32 v29, v29, v33
	v_add_f32_e32 v31, v28, v31
	v_add_f32_e32 v28, v28, v29
	v_add_f32_e32 v37, v32, v28
	v_rcp_f32_e32 v39, v37
	v_sub_f32_e32 v29, v32, v37
	v_add_f32_e32 v38, v28, v29
	v_add_f32_e32 v29, v30, v31
	v_mul_f32_e32 v41, v29, v39
	v_sub_f32_e32 v28, v30, v29
	v_mul_f32_e32 v30, v37, v41
	v_fma_f32 v32, v41, v37, -v30
	v_fmac_f32_e32 v32, v41, v38
	v_add_f32_e32 v40, v31, v28
	v_add_f32_e32 v28, v30, v32
	v_sub_f32_e32 v31, v29, v28
	v_pk_add_f32 v[34:35], v[28:29], v[30:31] neg_lo:[0,1] neg_hi:[0,1]
	v_mov_b32_e32 v33, v28
	v_pk_add_f32 v[28:29], v[34:35], v[32:33] neg_lo:[0,1] neg_hi:[0,1]
	v_cmp_neq_f32_e32 vcc, s94, v27
	v_add_f32_e32 v29, v40, v29
	v_add_f32_e32 v28, v28, v29
	v_add_f32_e32 v29, v31, v28
	v_mul_f32_e32 v40, v39, v29
	v_mul_f32_e32 v30, v37, v40
	v_fma_f32 v32, v40, v37, -v30
	v_fmac_f32_e32 v32, v40, v38
	v_sub_f32_e32 v31, v31, v29
	v_add_f32_e32 v37, v28, v31
	v_add_f32_e32 v28, v30, v32
	v_sub_f32_e32 v31, v29, v28
	v_pk_add_f32 v[34:35], v[28:29], v[30:31] neg_lo:[0,1] neg_hi:[0,1]
	v_mov_b32_e32 v33, v28
	v_pk_add_f32 v[28:29], v[34:35], v[32:33] neg_lo:[0,1] neg_hi:[0,1]
	s_nop 0
	v_add_f32_e32 v29, v37, v29
	v_add_f32_e32 v28, v28, v29
	v_add_f32_e32 v29, v41, v40
	v_add_f32_e32 v28, v31, v28
	v_sub_f32_e32 v30, v29, v41
	v_mul_f32_e32 v28, v39, v28
	v_sub_f32_e32 v30, v40, v30
	v_add_f32_e32 v30, v30, v28
	v_add_f32_e32 v32, v29, v30
	v_mul_f32_e32 v33, v32, v32
	v_fmamk_f32 v28, v33, 0x3e9b6dac, v182
	v_fmaak_f32 v107, v33, v28, 0x3f2aaada
	v_cvt_f32_i32_e32 v28, v36
	v_sub_f32_e32 v29, v32, v29
	v_sub_f32_e32 v29, v30, v29
	v_ldexp_f32 v34, v29, 1
	v_mul_f32_e32 v29, v32, v33
	v_ldexp_f32 v31, v32, 1
	v_pk_mul_f32 v[32:33], v[28:29], v[106:107]
	s_nop 0
	v_fma_f32 v30, v28, s11, -v32
	v_fmac_f32_e32 v30, 0xb102e308, v28
	v_pk_add_f32 v[28:29], v[32:33], v[30:31]
	s_nop 0
	v_sub_f32_e32 v31, v29, v31
	v_sub_f32_e32 v31, v33, v31
	v_add_f32_e32 v35, v34, v31
	v_mov_b32_e32 v34, v32
	v_pk_add_f32 v[32:33], v[28:29], v[32:33] neg_lo:[0,1] neg_hi:[0,1]
	v_pk_add_f32 v[36:37], v[28:29], v[34:35]
	v_mov_b32_e32 v31, v28
	v_mov_b32_e32 v33, v37
	v_pk_add_f32 v[38:39], v[30:31], v[32:33] neg_lo:[0,1] neg_hi:[0,1]
	v_pk_add_f32 v[30:31], v[30:31], v[32:33]
	v_mov_b32_e32 v42, v29
	v_pk_add_f32 v[32:33], v[30:31], v[28:29] op_sel:[1,0] op_sel_hi:[0,1] neg_lo:[0,1] neg_hi:[0,1]
	v_pk_add_f32 v[40:41], v[36:37], v[32:33] op_sel_hi:[1,0] neg_lo:[0,1] neg_hi:[0,1]
	v_mov_b32_e32 v36, v37
	v_mov_b32_e32 v37, v31
	v_mov_b32_e32 v43, v32
	v_pk_add_f32 v[32:33], v[36:37], v[42:43] neg_lo:[0,1] neg_hi:[0,1]
	v_mov_b32_e32 v34, v35
	v_mov_b32_e32 v35, v28
	v_pk_add_f32 v[28:29], v[34:35], v[32:33] neg_lo:[0,1] neg_hi:[0,1]
	v_mov_b32_e32 v40, v38
	v_pk_add_f32 v[32:33], v[40:41], v[28:29]
	v_mov_b32_e32 v39, v31
	v_pk_add_f32 v[34:35], v[32:33], v[32:33] op_sel:[0,1] op_sel_hi:[1,0]
	s_nop 0
	v_pk_add_f32 v[30:31], v[30:31], v[34:35] op_sel:[1,0] op_sel_hi:[0,1]
	v_mov_b32_e32 v33, v30
	v_pk_add_f32 v[36:37], v[32:33], v[38:39] neg_lo:[0,1] neg_hi:[0,1]
	v_mov_b32_e32 v29, v34
	v_sub_f32_e32 v31, v32, v36
	v_pk_add_f32 v[28:29], v[28:29], v[36:37] neg_lo:[0,1] neg_hi:[0,1]
	v_sub_f32_e32 v31, v38, v31
	v_add_f32_e32 v28, v28, v31
	v_add_f32_e32 v28, v28, v29
	v_add_f32_e32 v28, v30, v28
	v_cndmask_b32_e32 v28, v191, v28, vcc
	v_cmp_lt_f32_e64 vcc, |v27|, s76
	s_nop 1
	v_cndmask_b32_e32 v27, v28, v27, vcc
	v_xor_b32_e32 v108, 0x80000000, v27
.Llsv_ro1_a:
	s_xor_b64 exec, exec, s[98:99]
	s_cbranch_execz .Llsv_ro1_b
	v_mul_f32_e32 v27, 0x3fb8aa3b, v26
	v_rndne_f32_e32 v28, v27
	v_sub_f32_e32 v29, v27, v28
	v_fma_f32 v27, v26, s79, -v27
	v_fmac_f32_e32 v27, 0x32a5705f, v26
	v_add_f32_e32 v27, v29, v27
	v_cvt_i32_f32_e32 v28, v28
	v_exp_f32_e32 v27, v27
	s_mov_b32 s2, 0xc2ce8ed0
	v_cmp_ngt_f32_e32 vcc, s2, v26
	s_mov_b32 s2, 0x42b17218
	v_ldexp_f32 v27, v27, v28
	v_cndmask_b32_e32 v27, 0, v27, vcc
	v_cmp_nlt_f32_e32 vcc, s2, v26
	s_nop 1
	v_cndmask_b32_e32 v27, v191, v27, vcc
	v_add_f32_e32 v30, 1.0, v27
	v_add_f32_e32 v28, -1.0, v30
	v_sub_f32_e32 v29, v28, v30
	v_add_f32_e32 v29, 1.0, v29
	v_sub_f32_e32 v28, v27, v28
	v_add_f32_e32 v31, v28, v29
	v_frexp_mant_f32_e32 v32, v30
	v_cvt_f64_f32_e32 v[28:29], v30
	v_frexp_exp_i32_f64_e32 v28, v[28:29]
	v_cmp_gt_f32_e32 vcc, s78, v32
	s_nop 1
	v_subbrev_co_u32_e32 v36, vcc, 0, v28, vcc
	v_sub_u32_e32 v28, 0, v36
	v_ldexp_f32 v29, v30, v28
	v_add_f32_e32 v30, -1.0, v29
	v_add_f32_e32 v32, 1.0, v29
	v_ldexp_f32 v28, v31, v28
	v_add_f32_e32 v31, 1.0, v30
	v_add_f32_e32 v33, -1.0, v32
	v_sub_f32_e32 v31, v29, v31
	v_sub_f32_e32 v29, v29, v33
	v_add_f32_e32 v31, v28, v31
	v_add_f32_e32 v28, v28, v29
	v_add_f32_e32 v37, v32, v28
	v_rcp_f32_e32 v39, v37
	v_sub_f32_e32 v29, v32, v37
	v_add_f32_e32 v38, v28, v29
	v_add_f32_e32 v29, v30, v31
	v_mul_f32_e32 v41, v29, v39
	v_sub_f32_e32 v28, v30, v29
	v_mul_f32_e32 v30, v37, v41
	v_fma_f32 v32, v41, v37, -v30
	v_fmac_f32_e32 v32, v41, v38
	v_add_f32_e32 v40, v31, v28
	v_add_f32_e32 v28, v30, v32
	v_sub_f32_e32 v31, v29, v28
	v_pk_add_f32 v[34:35], v[28:29], v[30:31] neg_lo:[0,1] neg_hi:[0,1]
	v_mov_b32_e32 v33, v28
	v_pk_add_f32 v[28:29], v[34:35], v[32:33] neg_lo:[0,1] neg_hi:[0,1]
	v_cmp_neq_f32_e32 vcc, s94, v27
	v_add_f32_e32 v29, v40, v29
	v_add_f32_e32 v28, v28, v29
	v_add_f32_e32 v29, v31, v28
	v_mul_f32_e32 v40, v39, v29
	v_mul_f32_e32 v30, v37, v40
	v_fma_f32 v32, v40, v37, -v30
	v_fmac_f32_e32 v32, v40, v38
	v_sub_f32_e32 v31, v31, v29
	v_add_f32_e32 v37, v28, v31
	v_add_f32_e32 v28, v30, v32
	v_sub_f32_e32 v31, v29, v28
	v_pk_add_f32 v[34:35], v[28:29], v[30:31] neg_lo:[0,1] neg_hi:[0,1]
	v_mov_b32_e32 v33, v28
	v_pk_add_f32 v[28:29], v[34:35], v[32:33] neg_lo:[0,1] neg_hi:[0,1]
	s_nop 0
	v_add_f32_e32 v29, v37, v29
	v_add_f32_e32 v28, v28, v29
	v_add_f32_e32 v29, v41, v40
	v_add_f32_e32 v28, v31, v28
	v_sub_f32_e32 v30, v29, v41
	v_mul_f32_e32 v28, v39, v28
	v_sub_f32_e32 v30, v40, v30
	v_add_f32_e32 v30, v30, v28
	v_add_f32_e32 v32, v29, v30
	v_mul_f32_e32 v33, v32, v32
	v_fmamk_f32 v28, v33, 0x3e9b6dac, v182
	v_fmaak_f32 v107, v33, v28, 0x3f2aaada
	v_cvt_f32_i32_e32 v28, v36
	v_sub_f32_e32 v29, v32, v29
	v_sub_f32_e32 v29, v30, v29
	v_ldexp_f32 v34, v29, 1
	v_mul_f32_e32 v29, v32, v33
	v_ldexp_f32 v31, v32, 1
	v_pk_mul_f32 v[32:33], v[28:29], v[106:107]
	s_nop 0
	v_fma_f32 v30, v28, s11, -v32
	v_fmac_f32_e32 v30, 0xb102e308, v28
	v_pk_add_f32 v[28:29], v[32:33], v[30:31]
	s_nop 0
	v_sub_f32_e32 v31, v29, v31
	v_sub_f32_e32 v31, v33, v31
	v_add_f32_e32 v35, v34, v31
	v_mov_b32_e32 v34, v32
	v_pk_add_f32 v[32:33], v[28:29], v[32:33] neg_lo:[0,1] neg_hi:[0,1]
	v_pk_add_f32 v[36:37], v[28:29], v[34:35]
	v_mov_b32_e32 v31, v28
	v_mov_b32_e32 v33, v37
	v_pk_add_f32 v[38:39], v[30:31], v[32:33] neg_lo:[0,1] neg_hi:[0,1]
	v_pk_add_f32 v[30:31], v[30:31], v[32:33]
	v_mov_b32_e32 v42, v29
	v_pk_add_f32 v[32:33], v[30:31], v[28:29] op_sel:[1,0] op_sel_hi:[0,1] neg_lo:[0,1] neg_hi:[0,1]
	v_pk_add_f32 v[40:41], v[36:37], v[32:33] op_sel_hi:[1,0] neg_lo:[0,1] neg_hi:[0,1]
	v_mov_b32_e32 v36, v37
	v_mov_b32_e32 v37, v31
	v_mov_b32_e32 v43, v32
	v_pk_add_f32 v[32:33], v[36:37], v[42:43] neg_lo:[0,1] neg_hi:[0,1]
	v_mov_b32_e32 v34, v35
	v_mov_b32_e32 v35, v28
	v_pk_add_f32 v[28:29], v[34:35], v[32:33] neg_lo:[0,1] neg_hi:[0,1]
	v_mov_b32_e32 v40, v38
	v_pk_add_f32 v[32:33], v[40:41], v[28:29]
	v_mov_b32_e32 v39, v31
	v_pk_add_f32 v[34:35], v[32:33], v[32:33] op_sel:[0,1] op_sel_hi:[1,0]
	s_nop 0
	v_pk_add_f32 v[30:31], v[30:31], v[34:35] op_sel:[1,0] op_sel_hi:[0,1]
	v_mov_b32_e32 v33, v30
	v_pk_add_f32 v[36:37], v[32:33], v[38:39] neg_lo:[0,1] neg_hi:[0,1]
	v_mov_b32_e32 v29, v34
	v_sub_f32_e32 v31, v32, v36
	v_pk_add_f32 v[28:29], v[28:29], v[36:37] neg_lo:[0,1] neg_hi:[0,1]
	v_sub_f32_e32 v31, v38, v31
	v_add_f32_e32 v28, v28, v31
	v_add_f32_e32 v28, v28, v29
	v_add_f32_e32 v28, v30, v28
	v_cndmask_b32_e32 v28, v191, v28, vcc
	v_cmp_gt_f32_e32 vcc, s76, v27
	s_nop 1
	v_cndmask_b32_e32 v27, v28, v27, vcc
	v_sub_f32_e32 v108, v26, v27

.LBB0_3594:
	s_ashr_i32 s92, s86, 31
	s_lshr_b32 s0, s92, 27
	s_add_i32 s0, s86, s0
	s_ashr_i32 s93, s0, 5
	s_and_b32 s97, s93, 7
	s_lshl_b32 s0, s97, 2
	v_mov_b32_e32 v26, s0
	s_add_u32 s0, s82, s0
	s_addc_u32 s1, s83, 0
	s_waitcnt vmcnt(0)
	v_readlane_b32 vcc_lo, v222, s97
	s_add_i32 vcc_hi, s97, 8
	s_nop 1
	v_mov_b32_e32 v108, vcc_lo
	v_readlane_b32 vcc_lo, v222, vcc_hi
	s_nop 1
	v_mov_b32_e32 v107, vcc_lo

	.amdhsa_kernel _Z10fwd_kernelILin1EEv4Args
		.amdhsa_group_segment_fixed_size 0
		.amdhsa_private_segment_fixed_size 0
		.amdhsa_kernarg_size 520
		.amdhsa_user_sgpr_count 2
		.amdhsa_user_sgpr_dispatch_ptr 0
		.amdhsa_user_sgpr_queue_ptr 0
		.amdhsa_user_sgpr_kernarg_segment_ptr 1
		.amdhsa_user_sgpr_dispatch_id 0
		.amdhsa_user_sgpr_kernarg_preload_length 0
		.amdhsa_user_sgpr_kernarg_preload_offset 0
		.amdhsa_user_sgpr_private_segment_size 0
		.amdhsa_uses_dynamic_stack 0
		.amdhsa_enable_private_segment 0
		.amdhsa_system_sgpr_workgroup_id_x 1
		.amdhsa_system_sgpr_workgroup_id_y 0
		.amdhsa_system_sgpr_workgroup_id_z 0
		.amdhsa_system_sgpr_workgroup_info 0
		.amdhsa_system_vgpr_workitem_id 0
		.amdhsa_next_free_vgpr 240
		.amdhsa_next_free_sgpr 100
		.amdhsa_accum_offset 240
		.amdhsa_reserve_vcc 1
		.amdhsa_float_round_mode_32 0
		.amdhsa_float_round_mode_16_64 0
		.amdhsa_float_denorm_mode_32 3
		.amdhsa_float_denorm_mode_16_64 3
		.amdhsa_dx10_clamp 1
		.amdhsa_ieee_mode 1
		.amdhsa_fp16_overflow 0
		.amdhsa_tg_split 0
		.amdhsa_exception_fp_ieee_invalid_op 0
		.amdhsa_exception_fp_denorm_src 0
		.amdhsa_exception_fp_ieee_div_zero 0
		.amdhsa_exception_fp_ieee_overflow 0
		.amdhsa_exception_fp_ieee_underflow 0
		.amdhsa_exception_fp_ieee_inexact 0
		.amdhsa_exception_int_div_zero 0
	.end_amdhsa_kernel

amdhsa.kernels:
  - .agpr_count:     0
    .args:
      - .offset:         0
        .size:           264
        .value_kind:     by_value
      - .offset:         264
        .size:           4
        .value_kind:     hidden_block_count_x
      - .offset:         268
        .size:           4
        .value_kind:     hidden_block_count_y
      - .offset:         272
        .size:           4
        .value_kind:     hidden_block_count_z
      - .offset:         276
        .size:           2
        .value_kind:     hidden_group_size_x
      - .offset:         278
        .size:           2
        .value_kind:     hidden_group_size_y
      - .offset:         280
        .size:           2
        .value_kind:     hidden_group_size_z
      - .offset:         282
        .size:           2
        .value_kind:     hidden_remainder_x
      - .offset:         284
        .size:           2
        .value_kind:     hidden_remainder_y
      - .offset:         286
        .size:           2
        .value_kind:     hidden_remainder_z
      - .offset:         304
        .size:           8
        .value_kind:     hidden_global_offset_x
      - .offset:         312
        .size:           8
        .value_kind:     hidden_global_offset_y
      - .offset:         320
        .size:           8
        .value_kind:     hidden_global_offset_z
      - .offset:         328
        .size:           2
        .value_kind:     hidden_grid_dims
      - .offset:         384
        .size:           4
        .value_kind:     hidden_dynamic_lds_size
    .group_segment_fixed_size: 0
    .kernarg_segment_align: 8
    .kernarg_segment_size: 520
    .language:       OpenCL C
    .language_version:
      - 2
      - 0
    .max_flat_workgroup_size: 512
    .name:           _Z10fwd_kernelILin1EEv4Args
    .private_segment_fixed_size: 0
    .sgpr_count:     106
    .sgpr_spill_count: 135
    .symbol:         _Z10fwd_kernelILin1EEv4Args.kd
    .uniform_work_group_size: 1
    .uses_dynamic_stack: false
    .vgpr_count:     240
    .vgpr_spill_count: 0
    .wavefront_size: 64
